# v10 + latent attention: the DMA address add moved into the m0->LDS-DMA wait-state slot (42 sites, replaces s_nop 0)
# baseline (speedup 1.0000x reference)
; #define MLA_WAIT_BAR(N) asm volatile("s_waitcnt vmcnt(" #N ") lgkmcnt(0)\n\ts_barrier" ::: "memory")
; #define MLA_PIN(x) asm volatile("" : "+v"(x))
; #define MLA_LDK(kp, d0, h) (*(const __attribute__((address_space(3))) bf16x8*)((kp) + (d0) * 2048 + (h) * 512))
; #define MLA_MF(C, K, Q) C = __builtin_amdgcn_mfma_f32_32x32x16_bf16(K, Q, C, 0, 0, 0)
; template <int THRL, bool LATE> __device__ __forceinline__ void unit_stag(int b, int h, int qb, const unsigned short* Q, const unsigned short* KV, const unsigned short* KPE, unsigned short* O, char* shm, const int wave_) {
;     ...
;     glds16(ksrc, (unsigned)__builtin_amdgcn_readfirstlane(kdst)); if (lane < 32) glds16(psrc, (unsigned)__builtin_amdgcn_readfirstlane(pdst));
;     glds16(ksrc + (long)KVBLK * KVP, (unsigned)__builtin_amdgcn_readfirstlane(kdst + KSLOT)); if (lane < 32) glds16(psrc + (long)KVBLK * PEP, (unsigned)__builtin_amdgcn_readfirstlane(pdst + KSLOT)); glds16(vsrc, (unsigned)__builtin_amdgcn_readfirstlane(vdst));
;     glds16(ksrc + (long)2 * KVBLK * KVP, (unsigned)__builtin_amdgcn_readfirstlane(kdst + 2 * KSLOT)); if (lane < 32) glds16(psrc + (long)2 * KVBLK * PEP, (unsigned)__builtin_amdgcn_readfirstlane(pdst + 2 * KSLOT)); glds16(vsrc + (long)KVBLK * KVP, (unsigned)__builtin_amdgcn_readfirstlane(vdst + VSLOT));
;     float mhat = 0.f, l_reg = 0.f; f32x16 o[2]; o[0] = f32x16{}; o[1] = f32x16{}; f32x16 negm = f32x16{}; MLA_PIN(negm);
;     const int qrel = wid * QBLK + r32; bool resc = false;
;     f32x16 pA0, pA1, pB0, pB1; u32x4 pw0, pw1, pw2, pw3;
;     int s0 = 0, s1 = 1, s2 = 2;
;     MLA_WAIT_BAR(6);
;     { const lds_cptr kp = kp0;
;       pA0 = f32x16{}; pA1 = f32x16{};
; #pragma unroll
;       for (int d0 = 0; d0 < 6; ++d0) { const bf16x8 k0 = MLA_LDK(kp, d0, 0), k1 = MLA_LDK(kp, d0, 1); MLA_MF(pA0, k0, qr[d0]); MLA_MF(pA1, k1, qr[d0]); } }
;     { const float rm_ = rowmax(pA0, pA1); mhat = rm_;
; #pragma unroll
;       for (int r = 0; r < 16; ++r) { pA0[r] -= rm_; pA1[r] -= rm_; negm[r] = -mhat; }
;       MLA_PIN(negm); }
.LBB0_1097:
	s_or_b64 exec, exec, s[0:1]
	s_cmp_lg_u32 0, -1
	s_cselect_b32 s0, 0, 0
	s_add_i32 s0, s0, s42
	s_addk_i32 s0, 0x3000
	s_mov_b32 m0, s0
	v_lshl_add_u64 v[2:3], v[160:161], 0, s[12:13]
	global_load_lds_dwordx4 v[2:3], off
	s_and_saveexec_b64 s[0:1], s[2:3]
	s_cbranch_execz .LBB0_1099
	s_add_i32 s43, s71, 0x3000
	s_mov_b32 m0, s43
	v_lshl_add_u64 v[2:3], v[158:159], 0, s[14:15]
	global_load_lds_dwordx4 v[2:3], off
.LBB0_1099:
	s_or_b64 exec, exec, s[0:1]
	s_lshl_b32 s0, s68, 4
	v_lshrrev_b32_e32 v0, 2, v155
	v_and_or_b32 v0, s0, 48, v0
	s_ashr_i32 s0, s10, 3
	s_andn2_b32 s0, s0, 31
	s_ashr_i32 s1, s0, 31
	v_lshlrev_b32_e32 v168, 3, v82
	v_lshlrev_b32_e32 v0, 11, v0
	v_and_b32_e32 v83, 24, v168
	v_lshl_add_u64 v[2:3], s[36:37], 0, v[0:1]
	s_cmp_lg_u32 0, -1
	v_lshl_add_u64 v[2:3], s[0:1], 1, v[2:3]
	v_lshlrev_b32_e32 v0, 1, v83
	s_cselect_b32 s0, 0, 0
	v_lshl_add_u64 v[2:3], v[2:3], 0, v[0:1]
	s_add_i32 s0, s0, s42
	s_add_i32 s72, s0, 0x9000
	s_mov_b32 m0, s72
	v_lshl_add_u64 v[156:157], v[2:3], 0, s[16:17]
	global_load_lds_dwordx4 v[156:157], off
	s_addk_i32 s0, 0x6000
	s_mov_b32 m0, s0
	v_lshl_add_u64 v[2:3], v[160:161], 0, s[18:19]
	global_load_lds_dwordx4 v[2:3], off
	s_and_saveexec_b64 s[0:1], s[2:3]
	s_cbranch_execz .LBB0_1101
	s_add_i32 s43, s71, 0x6000
	s_mov_b32 m0, s43
	v_lshl_add_u64 v[2:3], v[158:159], 0, s[20:21]
	global_load_lds_dwordx4 v[2:3], off
.LBB0_1101:
	s_or_b64 exec, exec, s[0:1]
	s_cmp_lg_u32 0, -1
	v_lshlrev_b32_e32 v0, 10, v170
	v_lshlrev_b32_e32 v2, 4, v169
	s_cselect_b32 s0, 0, 0
	v_add3_u32 v173, 0, v0, v2
	s_add_i32 s0, s0, s42
	s_add_i32 s0, s0, 0xb000
	s_mov_b32 m0, s0
	v_lshl_add_u64 v[2:3], v[156:157], 0, s[12:13]
	global_load_lds_dwordx4 v[2:3], off
	v_mov_b32_e32 v2, v1
	v_mov_b32_e32 v3, v1
	v_mov_b32_e32 v4, v1
	v_mov_b32_e32 v5, v1
	v_mov_b32_e32 v6, v1
	v_mov_b32_e32 v7, v1
	v_mov_b32_e32 v8, v1
	v_mov_b32_e32 v9, v1
	v_mov_b32_e32 v10, v1
	v_mov_b32_e32 v11, v1
	v_mov_b32_e32 v12, v1
	v_mov_b32_e32 v13, v1
	v_mov_b32_e32 v14, v1
	v_mov_b32_e32 v15, v1
	v_mov_b32_e32 v0, v1
	v_mov_b64_e32 v[16:17], v[14:15]
	v_mov_b64_e32 v[14:15], v[12:13]
	v_mov_b64_e32 v[12:13], v[10:11]
	v_mov_b64_e32 v[10:11], v[8:9]
	v_mov_b64_e32 v[8:9], v[6:7]
	v_mov_b64_e32 v[6:7], v[4:5]
	v_mov_b64_e32 v[4:5], v[2:3]
	v_mov_b64_e32 v[2:3], v[0:1]
	s_waitcnt vmcnt(6) lgkmcnt(0)
	s_barrier
	ds_read_b128 v[2:5], v173
	ds_read_b128 v[6:9], v173 offset:512
	s_waitcnt vmcnt(5) lgkmcnt(1)
	v_mfma_f32_32x32x16_bf16 v[18:33], v[2:5], v[150:153], 0
	ds_read_b128 v[34:37], v173 offset:2048
	ds_read_b128 v[38:41], v173 offset:2560
	v_lshl_add_u64 v[50:51], v[160:161], 0, s[22:23]
	s_waitcnt lgkmcnt(2)
	v_mfma_f32_32x32x16_bf16 v[2:17], v[6:9], v[150:153], 0
	s_waitcnt vmcnt(4) lgkmcnt(1)
	v_mfma_f32_32x32x16_bf16 v[18:33], v[34:37], v[146:149], v[18:33]
	s_waitcnt lgkmcnt(0)
	v_mfma_f32_32x32x16_bf16 v[2:17], v[38:41], v[146:149], v[2:17]
	ds_read_b128 v[34:37], v173 offset:4096
	ds_read_b128 v[38:41], v173 offset:4608
	s_waitcnt vmcnt(3) lgkmcnt(1)
	v_mfma_f32_32x32x16_bf16 v[18:33], v[34:37], v[142:145], v[18:33]
	s_waitcnt lgkmcnt(0)
	v_mfma_f32_32x32x16_bf16 v[2:17], v[38:41], v[142:145], v[2:17]
	ds_read_b128 v[34:37], v173 offset:6144
	ds_read_b128 v[38:41], v173 offset:6656
	s_waitcnt vmcnt(2) lgkmcnt(1)
	v_mfma_f32_32x32x16_bf16 v[18:33], v[34:37], v[138:141], v[18:33]
	s_waitcnt lgkmcnt(0)
	v_mfma_f32_32x32x16_bf16 v[2:17], v[38:41], v[138:141], v[2:17]
	ds_read_b128 v[34:37], v173 offset:8192
	ds_read_b128 v[38:41], v173 offset:8704
	s_waitcnt vmcnt(1) lgkmcnt(1)
	v_mfma_f32_32x32x16_bf16 v[18:33], v[34:37], v[134:137], v[18:33]
	s_waitcnt lgkmcnt(0)
	v_mfma_f32_32x32x16_bf16 v[2:17], v[38:41], v[134:137], v[2:17]
	ds_read_b128 v[34:37], v173 offset:10240
	ds_read_b128 v[38:41], v173 offset:10752
	s_waitcnt vmcnt(0) lgkmcnt(1)
	v_mfma_f32_32x32x16_bf16 v[18:33], v[34:37], v[130:133], v[18:33]
	s_waitcnt lgkmcnt(0)
	v_mfma_f32_32x32x16_bf16 v[2:17], v[38:41], v[130:133], v[2:17]
	v_max3_f32 v0, v18, v19, v2
	v_max3_f32 v34, v20, v21, v3
	s_nop 0
	v_max3_f32 v0, v0, v4, v5
	v_max3_f32 v34, v34, v24, v25
	s_nop 0
	v_max3_f32 v0, v0, v22, v23
	v_max3_f32 v34, v34, v8, v9
	s_nop 0
	v_max3_f32 v0, v0, v6, v7
	v_max3_f32 v34, v34, v28, v29
	s_nop 0
	v_max3_f32 v0, v0, v26, v27
	v_max3_f32 v34, v34, v12, v13
	s_nop 0
	v_max3_f32 v0, v0, v10, v11
	v_max3_f32 v34, v34, v32, v33
	s_nop 0
	v_max3_f32 v0, v0, v30, v31
	v_max3_f32 v34, v34, v16, v17
	s_nop 0
	v_max3_f32 v0, v0, v14, v15
	v_max_f32_e32 v34, v34, v34
	v_max_f32_e32 v0, v0, v0
	v_max_f32_e32 v0, v0, v34
	v_mov_b32_e32 v34, v0
	s_nop 1
	v_permlane32_swap_b32_e32 v0, v34
	v_max_f32_e32 v34, v34, v34
	v_max_f32_e32 v0, v0, v0
	v_max_f32_e32 v154, v0, v34
	v_xor_b32_e32 v34, 0x80000000, v154
	v_mov_b32_e32 v35, v34
	v_mov_b32_e32 v36, v34
	v_mov_b32_e32 v37, v34
	v_mov_b32_e32 v38, v34
	v_mov_b32_e32 v39, v34
	v_mov_b32_e32 v40, v34
	v_mov_b32_e32 v41, v34
	v_mov_b32_e32 v42, v34
	v_mov_b32_e32 v43, v34
	v_mov_b32_e32 v44, v34
	v_mov_b32_e32 v45, v34
	v_mov_b32_e32 v46, v34
	v_mov_b32_e32 v47, v34
	v_mov_b32_e32 v48, v34
	v_mov_b32_e32 v49, v34
	s_waitcnt vmcnt(3) lgkmcnt(0)
	s_barrier
	s_mov_b32 m0, s76
	s_nop 0
	global_load_lds_dwordx4 v[50:51], off
	s_and_saveexec_b64 s[0:1], s[2:3]
	s_cbranch_execz .LBB0_1103
	s_mov_b32 m0, s71
	v_lshl_add_u64 v[50:51], v[158:159], 0, s[26:27]
	global_load_lds_dwordx4 v[50:51], off
.LBB0_1103:
	s_or_b64 exec, exec, s[0:1]
	s_and_b32 s0, s10, 0x3fffffc0
	s_lshl_b32 s0, s0, 2
	s_add_i32 s74, s0, 0
	s_add_i32 s74, s74, 0x11000
	s_cmp_lg_u32 0, -1
	s_cselect_b32 s0, 0, 0
	s_add_i32 s0, s0, s42
	v_sub_f32_e32 v96, v2, v154
	v_sub_f32_e32 v97, v3, v154
	s_add_i32 s0, s0, 0xd000
	s_mov_b32 m0, s0
	v_lshl_add_u64 v[2:3], v[156:157], 0, s[18:19]
	global_load_lds_dwordx4 v[2:3], off
	v_sub_f32_e32 v0, v18, v154
	v_sub_f32_e32 v19, v19, v154
	v_sub_f32_e32 v20, v20, v154
	v_sub_f32_e32 v98, v4, v154
	v_sub_f32_e32 v4, v21, v154
	v_sub_f32_e32 v99, v5, v154
	v_pk_add_f32 v[22:23], v[22:23], v[154:155] op_sel_hi:[1,0] neg_lo:[0,1] neg_hi:[0,1]
	v_pk_add_f32 v[6:7], v[6:7], v[154:155] op_sel_hi:[1,0] neg_lo:[0,1] neg_hi:[0,1]
	v_pk_add_f32 v[24:25], v[24:25], v[154:155] op_sel_hi:[1,0] neg_lo:[0,1] neg_hi:[0,1]
	v_pk_add_f32 v[8:9], v[8:9], v[154:155] op_sel_hi:[1,0] neg_lo:[0,1] neg_hi:[0,1]
	v_pk_add_f32 v[26:27], v[26:27], v[154:155] op_sel_hi:[1,0] neg_lo:[0,1] neg_hi:[0,1]
	v_pk_add_f32 v[10:11], v[10:11], v[154:155] op_sel_hi:[1,0] neg_lo:[0,1] neg_hi:[0,1]
	v_pk_add_f32 v[28:29], v[28:29], v[154:155] op_sel_hi:[1,0] neg_lo:[0,1] neg_hi:[0,1]
	v_pk_add_f32 v[12:13], v[12:13], v[154:155] op_sel_hi:[1,0] neg_lo:[0,1] neg_hi:[0,1]
	v_pk_add_f32 v[30:31], v[30:31], v[154:155] op_sel_hi:[1,0] neg_lo:[0,1] neg_hi:[0,1]
	v_pk_add_f32 v[14:15], v[14:15], v[154:155] op_sel_hi:[1,0] neg_lo:[0,1] neg_hi:[0,1]
	v_pk_add_f32 v[32:33], v[32:33], v[154:155] op_sel_hi:[1,0] neg_lo:[0,1] neg_hi:[0,1]
	v_pk_add_f32 v[16:17], v[16:17], v[154:155] op_sel_hi:[1,0] neg_lo:[0,1] neg_hi:[0,1]
	s_setprio 1
	v_exp_f32_e32 v21, v4
	ds_read_b128 v[2:5], v173 offset:12288
	ds_read_b128 v[84:87], v173 offset:12800
	v_exp_f32_e32 v18, v0
	v_exp_f32_e32 v19, v19
	v_exp_f32_e32 v20, v20
	s_nop 0
	v_exp_f32_e32 v22, v22
	v_exp_f32_e32 v23, v23
	v_exp_f32_e32 v24, v24
	v_exp_f32_e32 v25, v25
	s_waitcnt lgkmcnt(1)
	v_mfma_f32_32x32x16_bf16 v[66:81], v[2:5], v[150:153], v[34:49]
	ds_read_b128 v[88:91], v173 offset:14336
	ds_read_b128 v[92:95], v173 offset:14848
	v_exp_f32_e32 v26, v26
	v_exp_f32_e32 v27, v27
	v_exp_f32_e32 v28, v28
	v_exp_f32_e32 v29, v29
	v_mov_b64_e32 v[64:65], v[48:49]
	v_mov_b64_e32 v[62:63], v[46:47]
	v_mov_b64_e32 v[60:61], v[44:45]
	v_mov_b64_e32 v[58:59], v[42:43]
	v_mov_b64_e32 v[56:57], v[40:41]
	v_mov_b64_e32 v[54:55], v[38:39]
	v_mov_b64_e32 v[52:53], v[36:37]
	v_mov_b64_e32 v[50:51], v[34:35]
	v_exp_f32_e32 v30, v30
	v_exp_f32_e32 v31, v31
	s_waitcnt lgkmcnt(2)
	v_mfma_f32_32x32x16_bf16 v[50:65], v[84:87], v[150:153], v[50:65]
	v_exp_f32_e32 v32, v32
	v_exp_f32_e32 v33, v33
	s_nop 0
	v_add_f32_e32 v0, 0, v18
	v_add_f32_e32 v0, v19, v0
	v_add_f32_e32 v0, v20, v0
	v_add_f32_e32 v0, v21, v0
	s_waitcnt lgkmcnt(1)
	v_mfma_f32_32x32x16_bf16 v[66:81], v[88:91], v[146:149], v[66:81]
	v_exp_f32_e32 v2, v96
	v_exp_f32_e32 v3, v97
	v_exp_f32_e32 v4, v98
	v_exp_f32_e32 v5, v99
	ds_read_b128 v[84:87], v173 offset:16384
	ds_read_b128 v[96:99], v173 offset:16896
	v_add_f32_e32 v0, v0, v22
	v_add_f32_e32 v0, v23, v0
	v_add_f32_e32 v0, v24, v0
	v_add_f32_e32 v0, v25, v0
	s_waitcnt lgkmcnt(2)
	v_mfma_f32_32x32x16_bf16 v[50:65], v[92:95], v[146:149], v[50:65]
	v_add_f32_e32 v0, v26, v0
	v_add_f32_e32 v0, v27, v0
	v_add_f32_e32 v0, v28, v0
	v_exp_f32_e32 v6, v6
	v_exp_f32_e32 v7, v7
	v_exp_f32_e32 v8, v8
	v_exp_f32_e32 v9, v9
	v_add_f32_e32 v0, v29, v0
	v_cvt_pk_bf16_f32 v114, v18, v19
	v_cvt_pk_bf16_f32 v115, v20, v21
	s_waitcnt lgkmcnt(1)
	v_mfma_f32_32x32x16_bf16 v[66:81], v[84:87], v[142:145], v[66:81]
	ds_read_b128 v[18:21], v173 offset:18432
	ds_read_b128 v[88:91], v173 offset:18944
	v_add_f32_e32 v0, v30, v0
	v_add_f32_e32 v0, v31, v0
	v_add_f32_e32 v0, v32, v0
	v_exp_f32_e32 v10, v10
	v_exp_f32_e32 v11, v11
	v_exp_f32_e32 v12, v12
	v_exp_f32_e32 v13, v13
	v_add_f32_e32 v0, v33, v0
	v_cvt_pk_bf16_f32 v116, v22, v23
	v_cvt_pk_bf16_f32 v117, v24, v25
	s_waitcnt lgkmcnt(2)
	v_mfma_f32_32x32x16_bf16 v[50:65], v[96:99], v[142:145], v[50:65]
	v_exp_f32_e32 v14, v14
	v_exp_f32_e32 v15, v15
	v_exp_f32_e32 v16, v16
	v_exp_f32_e32 v17, v17
	v_cvt_pk_bf16_f32 v118, v26, v27
	v_add_f32_e32 v0, v0, v2
	v_add_f32_e32 v0, v3, v0
	v_add_f32_e32 v0, v4, v0
	v_add_f32_e32 v0, v5, v0
	v_cvt_pk_bf16_f32 v119, v28, v29
	s_waitcnt lgkmcnt(1)
	v_mfma_f32_32x32x16_bf16 v[66:81], v[18:21], v[138:141], v[66:81]
	ds_read_b128 v[22:25], v173 offset:20480
	ds_read_b128 v[26:29], v173 offset:20992
	v_add_f32_e32 v0, v0, v6
	v_add_f32_e32 v0, v7, v0
	v_add_f32_e32 v0, v8, v0
	v_add_f32_e32 v0, v9, v0
	v_cvt_pk_bf16_f32 v120, v30, v31
	v_cvt_pk_bf16_f32 v121, v32, v33
	s_waitcnt lgkmcnt(2)
	v_mfma_f32_32x32x16_bf16 v[50:65], v[88:91], v[138:141], v[50:65]
	v_add_f32_e32 v0, v10, v0
	v_add_f32_e32 v0, v11, v0
	v_add_f32_e32 v0, v12, v0
	v_add_f32_e32 v0, v13, v0
	v_cvt_pk_bf16_f32 v122, v2, v3
	v_cvt_pk_bf16_f32 v123, v4, v5
	s_waitcnt lgkmcnt(1)
	v_mfma_f32_32x32x16_bf16 v[66:81], v[22:25], v[134:137], v[66:81]
	ds_read_b128 v[2:5], v173 offset:22528
	ds_read_b128 v[18:21], v173 offset:23040
	v_add_f32_e32 v0, v14, v0
	v_add_f32_e32 v0, v15, v0
	v_add_f32_e32 v0, v16, v0
	v_add_f32_e32 v0, v17, v0
	v_cvt_pk_bf16_f32 v124, v6, v7
	v_cvt_pk_bf16_f32 v125, v8, v9
	s_waitcnt lgkmcnt(2)
	v_mfma_f32_32x32x16_bf16 v[50:65], v[26:29], v[134:137], v[50:65]
	v_cvt_pk_bf16_f32 v126, v10, v11
	v_cvt_pk_bf16_f32 v127, v12, v13
	s_waitcnt lgkmcnt(1)
	v_mfma_f32_32x32x16_bf16 v[66:81], v[2:5], v[130:133], v[66:81]
	v_cvt_pk_bf16_f32 v128, v14, v15
	v_cvt_pk_bf16_f32 v129, v16, v17
	s_waitcnt lgkmcnt(0)
	v_mfma_f32_32x32x16_bf16 v[50:65], v[18:21], v[130:133], v[50:65]
	v_add_f32_e32 v175, 0, v0
	s_setprio 0
	v_max3_f32 v0, v66, v67, v50
	v_max3_f32 v2, v68, v69, v51
	s_nop 0
	v_max3_f32 v0, v0, v52, v53
	v_max3_f32 v2, v2, v72, v73
	s_nop 0
	v_max3_f32 v0, v0, v70, v71
	v_max3_f32 v2, v2, v56, v57
	s_nop 0
	v_max3_f32 v0, v0, v54, v55
	v_max3_f32 v2, v2, v76, v77
	s_nop 0
	v_max3_f32 v0, v0, v74, v75
	v_max3_f32 v2, v2, v60, v61
	s_nop 0
	v_max3_f32 v0, v0, v58, v59
	v_max3_f32 v2, v2, v80, v81
	s_nop 0
	v_max3_f32 v0, v0, v78, v79
	v_max3_f32 v2, v2, v64, v65
	s_nop 0
	v_max3_f32 v0, v0, v62, v63
	v_max_f32_e32 v2, v2, v2
	v_max_f32_e32 v0, v0, v0
	v_max_f32_e32 v0, v0, v2
	v_mov_b32_e32 v2, v0
	s_nop 1
	v_permlane32_swap_b32_e32 v0, v2
	v_max_f32_e32 v2, v2, v2
	v_max_f32_e32 v0, v0, v0
	v_max_f32_e32 v0, v0, v2
	v_cmp_lt_f32_e32 vcc, s54, v0
	s_cmp_lg_u64 vcc, 0
	s_cselect_b64 s[42:43], -1, 0
	s_cbranch_vccnz .LBB0_1205

.LBB0_1107:
	v_lshl_add_u64 v[164:165], v[160:161], 0, s[0:1]
	s_mul_i32 s77, s81, 0x3000
	s_add_i32 s78, s77, s76
	s_mov_b32 m0, s78
	v_lshl_add_u64 v[82:83], v[164:165], 0, s[12:13]
	global_load_lds_dwordx4 v[82:83], off
	s_and_saveexec_b64 s[42:43], s[2:3]
	s_cbranch_execz .LBB0_1109
	s_add_i32 s44, s77, s71
	s_mov_b32 m0, s44
	v_lshl_add_u64 v[82:83], v[162:163], 0, s[30:31]
	global_load_lds_dwordx4 v[82:83], off
.LBB0_1109:
	s_or_b64 exec, exec, s[42:43]
	s_add_i32 s42, s82, 0xffffe000
	s_and_b32 s70, s42, 0x6000
	s_add_i32 s73, s70, s72
	s_mov_b32 m0, s73
	v_lshl_add_u64 v[166:167], v[156:157], 0, s[0:1]
	global_load_lds_dwordx4 v[166:167], off
	s_mul_i32 s86, s83, 0x3000
	v_add_u32_e32 v185, s86, v173
	s_setprio 1
	ds_read_b128 v[82:85], v185
	ds_read_b128 v[176:179], v185 offset:512
	v_exp_f32_e32 v66, v66
	v_exp_f32_e32 v67, v67
	v_exp_f32_e32 v68, v68
	v_exp_f32_e32 v69, v69
	s_nop 0
	v_exp_f32_e32 v70, v70
	v_exp_f32_e32 v71, v71
	v_exp_f32_e32 v72, v72
	v_exp_f32_e32 v73, v73
	s_waitcnt lgkmcnt(1)
	v_mfma_f32_32x32x16_bf16 v[98:113], v[82:85], v[150:153], v[34:49]
	ds_read_b128 v[186:189], v185 offset:2048
	ds_read_b128 v[190:193], v185 offset:2560
	v_exp_f32_e32 v74, v74
	v_exp_f32_e32 v75, v75
	v_exp_f32_e32 v76, v76
	v_exp_f32_e32 v77, v77
	s_waitcnt lgkmcnt(2)
	v_mfma_f32_32x32x16_bf16 v[82:97], v[176:179], v[150:153], v[34:49]
	v_exp_f32_e32 v78, v78
	v_exp_f32_e32 v79, v79
	v_exp_f32_e32 v80, v80
	v_exp_f32_e32 v81, v81
	s_nop 0
	v_add_f32_e32 v0, 0, v66
	v_add_f32_e32 v0, v67, v0
	v_add_f32_e32 v0, v68, v0
	v_add_f32_e32 v0, v69, v0
	s_waitcnt lgkmcnt(1)
	v_mfma_f32_32x32x16_bf16 v[98:113], v[186:189], v[146:149], v[98:113]
	ds_read_b128 v[176:179], v185 offset:4096
	ds_read_b128 v[194:197], v185 offset:4608
	v_add_f32_e32 v0, v0, v70
	v_add_f32_e32 v0, v71, v0
	v_add_f32_e32 v0, v72, v0
	v_exp_f32_e32 v50, v50
	v_exp_f32_e32 v51, v51
	v_exp_f32_e32 v52, v52
	v_exp_f32_e32 v53, v53
	v_add_f32_e32 v0, v73, v0
	s_waitcnt lgkmcnt(2)
	v_mfma_f32_32x32x16_bf16 v[82:97], v[190:193], v[146:149], v[82:97]
	v_add_f32_e32 v0, v74, v0
	v_add_f32_e32 v0, v75, v0
	v_add_f32_e32 v0, v76, v0
	v_exp_f32_e32 v54, v54
	v_exp_f32_e32 v55, v55
	v_exp_f32_e32 v56, v56
	v_exp_f32_e32 v57, v57
	v_add_f32_e32 v0, v77, v0
	v_cvt_pk_bf16_f32 v114, v66, v67
	v_cvt_pk_bf16_f32 v115, v68, v69
	s_waitcnt lgkmcnt(1)
	v_mfma_f32_32x32x16_bf16 v[98:113], v[176:179], v[142:145], v[98:113]
	ds_read_b128 v[66:69], v185 offset:6144
	ds_read_b128 v[186:189], v185 offset:6656
	v_add_f32_e32 v0, v78, v0
	v_add_f32_e32 v0, v79, v0
	v_add_f32_e32 v0, v80, v0
	v_exp_f32_e32 v58, v58
	v_exp_f32_e32 v59, v59
	v_exp_f32_e32 v60, v60
	v_exp_f32_e32 v61, v61
	v_add_f32_e32 v0, v81, v0
	v_cvt_pk_bf16_f32 v116, v70, v71
	v_cvt_pk_bf16_f32 v117, v72, v73
	s_waitcnt lgkmcnt(2)
	v_mfma_f32_32x32x16_bf16 v[82:97], v[194:197], v[142:145], v[82:97]
	v_exp_f32_e32 v62, v62
	v_exp_f32_e32 v63, v63
	v_exp_f32_e32 v64, v64
	v_exp_f32_e32 v65, v65
	v_cvt_pk_bf16_f32 v118, v74, v75
	v_add_f32_e32 v0, v0, v50
	v_add_f32_e32 v0, v51, v0
	v_add_f32_e32 v0, v52, v0
	v_add_f32_e32 v0, v53, v0
	v_cvt_pk_bf16_f32 v119, v76, v77
	s_waitcnt lgkmcnt(1)
	v_mfma_f32_32x32x16_bf16 v[98:113], v[66:69], v[138:141], v[98:113]
	ds_read_b128 v[70:73], v185 offset:8192
	ds_read_b128 v[74:77], v185 offset:8704
	v_add_f32_e32 v0, v0, v54
	v_add_f32_e32 v0, v55, v0
	v_add_f32_e32 v0, v56, v0
	v_add_f32_e32 v0, v57, v0
	v_cvt_pk_bf16_f32 v120, v78, v79
	v_cvt_pk_bf16_f32 v121, v80, v81
	s_waitcnt lgkmcnt(2)
	v_mfma_f32_32x32x16_bf16 v[82:97], v[186:189], v[138:141], v[82:97]
	v_add_f32_e32 v0, v58, v0
	v_add_f32_e32 v0, v59, v0
	v_add_f32_e32 v0, v60, v0
	v_add_f32_e32 v0, v61, v0
	v_cvt_pk_bf16_f32 v122, v50, v51
	v_cvt_pk_bf16_f32 v123, v52, v53
	s_waitcnt lgkmcnt(1)
	v_mfma_f32_32x32x16_bf16 v[98:113], v[70:73], v[134:137], v[98:113]
	ds_read_b128 v[50:53], v185 offset:10240
	ds_read_b128 v[66:69], v185 offset:10752
	v_add_f32_e32 v0, v62, v0
	v_add_f32_e32 v0, v63, v0
	v_add_f32_e32 v0, v64, v0
	v_add_f32_e32 v0, v65, v0
	v_cvt_pk_bf16_f32 v124, v54, v55
	v_cvt_pk_bf16_f32 v125, v56, v57
	s_waitcnt lgkmcnt(2)
	v_mfma_f32_32x32x16_bf16 v[82:97], v[74:77], v[134:137], v[82:97]
	v_cvt_pk_bf16_f32 v126, v58, v59
	v_cvt_pk_bf16_f32 v127, v60, v61
	s_waitcnt lgkmcnt(1)
	v_mfma_f32_32x32x16_bf16 v[98:113], v[50:53], v[130:133], v[98:113]
	v_cvt_pk_bf16_f32 v128, v62, v63
	v_cvt_pk_bf16_f32 v129, v64, v65
	s_waitcnt lgkmcnt(0)
	v_mfma_f32_32x32x16_bf16 v[82:97], v[66:69], v[130:133], v[82:97]
	v_add_f32_e32 v0, v175, v0
	s_setprio 0
	v_max3_f32 v50, v98, v99, v82
	v_max3_f32 v51, v100, v101, v83
	s_nop 0
	v_max3_f32 v50, v50, v84, v85
	v_max3_f32 v51, v51, v104, v105
	s_nop 0
	v_max3_f32 v50, v50, v102, v103
	v_max3_f32 v51, v51, v88, v89
	s_nop 0
	v_max3_f32 v50, v50, v86, v87
	v_max3_f32 v51, v51, v108, v109
	s_nop 0
	v_max3_f32 v50, v50, v106, v107
	v_max3_f32 v51, v51, v92, v93
	s_nop 0
	v_max3_f32 v50, v50, v90, v91
	v_max3_f32 v51, v51, v112, v113
	s_nop 0
	v_max3_f32 v50, v50, v110, v111
	v_max3_f32 v51, v51, v96, v97
	s_nop 0
	v_max3_f32 v50, v50, v94, v95
	v_max_f32_e32 v51, v51, v51
	v_max_f32_e32 v50, v50, v50
	v_max_f32_e32 v50, v50, v51
	v_mov_b32_e32 v51, v50
	s_nop 1
	v_permlane32_swap_b32_e32 v50, v51
	v_max_f32_e32 v51, v51, v51
	v_max_f32_e32 v50, v50, v50
	v_max_f32_e32 v50, v50, v51
	v_cmp_lt_f32_e32 vcc, s54, v50
	s_cmp_lg_u64 vcc, 0
	s_cselect_b64 s[42:43], -1, 0
	s_cbranch_vccnz .LBB0_1117

.LBB0_1112:
	s_add_i32 s42, s86, s76
	s_mov_b32 m0, s42
	v_lshl_add_u64 v[50:51], v[164:165], 0, s[18:19]
	global_load_lds_dwordx4 v[50:51], off
	s_and_saveexec_b64 s[42:43], s[2:3]
	s_cbranch_execz .LBB0_1114
	s_add_i32 s44, s86, s71
	s_mov_b32 m0, s44
	s_nop 0
	global_load_lds_dwordx4 v[162:163], off
.LBB0_1114:
	s_or_b64 exec, exec, s[42:43]
	s_add_i32 s42, s84, s72
	s_mov_b32 m0, s42
	v_lshl_add_u64 v[50:51], v[166:167], 0, s[12:13]
	global_load_lds_dwordx4 v[50:51], off
	s_mul_i32 s86, s10, 0x3000
	v_add_u32_e32 v184, s86, v173
	s_setprio 1
	ds_read_b128 v[50:53], v184
	ds_read_b128 v[164:167], v184 offset:512
	v_exp_f32_e32 v98, v98
	v_exp_f32_e32 v99, v99
	v_exp_f32_e32 v100, v100
	v_exp_f32_e32 v101, v101
	s_nop 0
	v_exp_f32_e32 v102, v102
	v_exp_f32_e32 v103, v103
	v_exp_f32_e32 v104, v104
	v_exp_f32_e32 v105, v105
	s_waitcnt lgkmcnt(1)
	v_mfma_f32_32x32x16_bf16 v[66:81], v[50:53], v[150:153], v[34:49]
	ds_read_b128 v[176:179], v184 offset:2048
	ds_read_b128 v[186:189], v184 offset:2560
	v_exp_f32_e32 v106, v106
	v_exp_f32_e32 v107, v107
	v_exp_f32_e32 v108, v108
	v_exp_f32_e32 v109, v109
	s_waitcnt lgkmcnt(2)
	v_mfma_f32_32x32x16_bf16 v[50:65], v[164:167], v[150:153], v[34:49]
	v_exp_f32_e32 v110, v110
	v_exp_f32_e32 v111, v111
	v_exp_f32_e32 v112, v112
	v_exp_f32_e32 v113, v113
	s_nop 0
	v_add_f32_e32 v114, 0, v98
	v_add_f32_e32 v114, v99, v114
	v_add_f32_e32 v114, v100, v114
	v_add_f32_e32 v114, v101, v114
	s_waitcnt lgkmcnt(1)
	v_mfma_f32_32x32x16_bf16 v[66:81], v[176:179], v[146:149], v[66:81]
	ds_read_b128 v[164:167], v184 offset:4096
	ds_read_b128 v[190:193], v184 offset:4608
	v_add_f32_e32 v114, v114, v102
	v_add_f32_e32 v114, v103, v114
	v_add_f32_e32 v114, v104, v114
	v_exp_f32_e32 v82, v82
	v_exp_f32_e32 v83, v83
	v_exp_f32_e32 v84, v84
	v_exp_f32_e32 v85, v85
	v_add_f32_e32 v114, v105, v114
	s_waitcnt lgkmcnt(2)
	v_mfma_f32_32x32x16_bf16 v[50:65], v[186:189], v[146:149], v[50:65]
	v_add_f32_e32 v114, v106, v114
	v_add_f32_e32 v114, v107, v114
	v_add_f32_e32 v114, v108, v114
	v_exp_f32_e32 v86, v86
	v_exp_f32_e32 v87, v87
	v_exp_f32_e32 v88, v88
	v_exp_f32_e32 v89, v89
	v_add_f32_e32 v118, v109, v114
	v_cvt_pk_bf16_f32 v114, v98, v99
	v_cvt_pk_bf16_f32 v115, v100, v101
	s_waitcnt lgkmcnt(1)
	v_mfma_f32_32x32x16_bf16 v[66:81], v[164:167], v[142:145], v[66:81]
	ds_read_b128 v[98:101], v184 offset:6144
	ds_read_b128 v[176:179], v184 offset:6656
	v_add_f32_e32 v116, v110, v118
	v_add_f32_e32 v116, v111, v116
	v_add_f32_e32 v116, v112, v116
	v_exp_f32_e32 v90, v90
	v_exp_f32_e32 v91, v91
	v_exp_f32_e32 v92, v92
	v_exp_f32_e32 v93, v93
	v_add_f32_e32 v118, v113, v116
	v_cvt_pk_bf16_f32 v116, v102, v103
	v_cvt_pk_bf16_f32 v117, v104, v105
	s_waitcnt lgkmcnt(2)
	v_mfma_f32_32x32x16_bf16 v[50:65], v[190:193], v[142:145], v[50:65]
	v_exp_f32_e32 v94, v94
	v_exp_f32_e32 v95, v95
	v_exp_f32_e32 v96, v96
	v_exp_f32_e32 v97, v97
	v_cvt_pk_bf16_f32 v119, v108, v109
	v_add_f32_e32 v102, v118, v82
	v_add_f32_e32 v102, v83, v102
	v_add_f32_e32 v102, v84, v102
	v_add_f32_e32 v122, v85, v102
	v_cvt_pk_bf16_f32 v118, v106, v107
	s_waitcnt lgkmcnt(1)
	v_mfma_f32_32x32x16_bf16 v[66:81], v[98:101], v[138:141], v[66:81]
	ds_read_b128 v[102:105], v184 offset:8192
	ds_read_b128 v[106:109], v184 offset:8704
	v_add_f32_e32 v120, v122, v86
	v_add_f32_e32 v120, v87, v120
	v_add_f32_e32 v120, v88, v120
	v_add_f32_e32 v122, v89, v120
	v_cvt_pk_bf16_f32 v120, v110, v111
	v_cvt_pk_bf16_f32 v121, v112, v113
	s_waitcnt lgkmcnt(2)
	v_mfma_f32_32x32x16_bf16 v[50:65], v[176:179], v[138:141], v[50:65]
	v_add_f32_e32 v98, v90, v122
	v_add_f32_e32 v98, v91, v98
	v_add_f32_e32 v98, v92, v98
	v_add_f32_e32 v110, v93, v98
	v_cvt_pk_bf16_f32 v122, v82, v83
	v_cvt_pk_bf16_f32 v123, v84, v85
	s_waitcnt lgkmcnt(1)
	v_mfma_f32_32x32x16_bf16 v[66:81], v[102:105], v[134:137], v[66:81]
	ds_read_b128 v[82:85], v184 offset:10240
	ds_read_b128 v[98:101], v184 offset:10752
	v_add_f32_e32 v110, v94, v110
	v_add_f32_e32 v110, v95, v110
	v_add_f32_e32 v110, v96, v110
	v_add_f32_e32 v110, v97, v110
	v_cvt_pk_bf16_f32 v124, v86, v87
	v_cvt_pk_bf16_f32 v125, v88, v89
	s_waitcnt lgkmcnt(2)
	v_mfma_f32_32x32x16_bf16 v[50:65], v[106:109], v[134:137], v[50:65]
	v_cvt_pk_bf16_f32 v126, v90, v91
	v_cvt_pk_bf16_f32 v127, v92, v93
	s_waitcnt lgkmcnt(1)
	v_mfma_f32_32x32x16_bf16 v[66:81], v[82:85], v[130:133], v[66:81]
	v_cvt_pk_bf16_f32 v128, v94, v95
	v_cvt_pk_bf16_f32 v129, v96, v97
	s_waitcnt lgkmcnt(0)
	v_mfma_f32_32x32x16_bf16 v[50:65], v[98:101], v[130:133], v[50:65]
	v_add_f32_e32 v175, v0, v110
	s_setprio 0
	v_max3_f32 v0, v66, v67, v50
	v_max3_f32 v82, v68, v69, v51
	s_nop 0
	v_max3_f32 v0, v0, v52, v53
	v_max3_f32 v82, v82, v72, v73
	s_nop 0
	v_max3_f32 v0, v0, v70, v71
	v_max3_f32 v82, v82, v56, v57
	s_nop 0
	v_max3_f32 v0, v0, v54, v55
	v_max3_f32 v82, v82, v76, v77
	s_nop 0
	v_max3_f32 v0, v0, v74, v75
	v_max3_f32 v82, v82, v60, v61
	s_nop 0
	v_max3_f32 v0, v0, v58, v59
	v_max3_f32 v82, v82, v80, v81
	s_nop 0
	v_max3_f32 v0, v0, v78, v79
	v_max3_f32 v82, v82, v64, v65
	s_nop 0
	v_max3_f32 v0, v0, v62, v63
	v_max_f32_e32 v82, v82, v82
	v_max_f32_e32 v0, v0, v0
	v_max_f32_e32 v0, v0, v82
	v_mov_b32_e32 v82, v0
	s_nop 1
	v_permlane32_swap_b32_e32 v0, v82
	v_max_f32_e32 v82, v82, v82
	v_max_f32_e32 v0, v0, v0
	v_max_f32_e32 v0, v0, v82
	v_cmp_lt_f32_e32 vcc, s54, v0
	s_cmp_lg_u64 vcc, 0
	s_cselect_b64 s[42:43], -1, 0
	s_cbranch_vccnz .LBB0_1120

.LBB0_1126:
	s_lshl_b64 s[42:43], s[10:11], 17
	s_add_i32 s44, s86, s76
	s_mov_b32 m0, s44
	v_lshl_add_u64 v[82:83], v[160:161], 0, s[42:43]
	global_load_lds_dwordx4 v[82:83], off
	s_and_saveexec_b64 s[44:45], s[2:3]
	s_cbranch_execz .LBB0_1128
	s_lshl_b64 s[80:81], s[10:11], 12
	s_add_i32 s76, s86, s71
	s_mov_b32 m0, s76
	v_lshl_add_u64 v[82:83], v[158:159], 0, s[80:81]
	global_load_lds_dwordx4 v[82:83], off

.LBB0_1131:
	s_add_i32 s10, s84, 6
	s_lshl_b64 s[0:1], s[10:11], 17
	s_mov_b32 m0, s78
	v_lshl_add_u64 v[82:83], v[160:161], 0, s[0:1]
	global_load_lds_dwordx4 v[82:83], off
	s_and_saveexec_b64 s[44:45], s[2:3]
	s_cbranch_execz .LBB0_1133
	s_lshl_b64 s[74:75], s[10:11], 12
	s_add_i32 s71, s77, s71
	s_mov_b32 m0, s71
	v_lshl_add_u64 v[82:83], v[158:159], 0, s[74:75]
	global_load_lds_dwordx4 v[82:83], off
.LBB0_1133:
	s_or_b64 exec, exec, s[44:45]
	s_add_i32 s10, s79, s72
	s_mov_b32 m0, s10
	v_lshl_add_u64 v[82:83], v[156:157], 0, s[42:43]
	global_load_lds_dwordx4 v[82:83], off
	s_setprio 1
	ds_read_b128 v[98:101], v185
	ds_read_b128 v[158:161], v185 offset:512
	v_exp_f32_e32 v66, v66
	v_exp_f32_e32 v67, v67
	v_exp_f32_e32 v68, v68
	v_exp_f32_e32 v69, v69
	s_nop 0
	v_exp_f32_e32 v70, v70
	v_exp_f32_e32 v71, v71
	v_exp_f32_e32 v72, v72
	v_exp_f32_e32 v73, v73
	s_waitcnt lgkmcnt(1)
	v_mfma_f32_32x32x16_bf16 v[82:97], v[98:101], v[150:153], v[34:49]
	ds_read_b128 v[188:191], v185 offset:2048
	ds_read_b128 v[192:195], v185 offset:2560
	v_exp_f32_e32 v74, v74
	v_exp_f32_e32 v75, v75
	v_exp_f32_e32 v76, v76
	v_exp_f32_e32 v77, v77
	s_nop 0
	v_exp_f32_e32 v78, v78
	v_exp_f32_e32 v79, v79
	v_exp_f32_e32 v80, v80
	v_exp_f32_e32 v81, v81
	s_waitcnt lgkmcnt(2)
	v_mfma_f32_32x32x16_bf16 v[98:113], v[158:161], v[150:153], v[34:49]
	v_add_f32_e32 v114, 0, v66
	v_add_f32_e32 v114, v67, v114
	v_add_f32_e32 v114, v68, v114
	v_add_f32_e32 v114, v69, v114
	s_waitcnt lgkmcnt(1)
	v_mfma_f32_32x32x16_bf16 v[82:97], v[188:191], v[146:149], v[82:97]
	ds_read_b128 v[158:161], v185 offset:4096
	ds_read_b128 v[196:199], v185 offset:4608
	v_add_f32_e32 v114, v114, v70
	v_add_f32_e32 v114, v71, v114
	v_add_f32_e32 v114, v72, v114
	v_exp_f32_e32 v50, v50
	v_exp_f32_e32 v51, v51
	v_exp_f32_e32 v52, v52
	v_exp_f32_e32 v53, v53
	v_add_f32_e32 v114, v73, v114
	s_nop 0
	v_add_f32_e32 v114, v74, v114
	v_add_f32_e32 v114, v75, v114
	v_add_f32_e32 v114, v76, v114
	v_exp_f32_e32 v54, v54
	v_exp_f32_e32 v55, v55
	v_exp_f32_e32 v56, v56
	v_exp_f32_e32 v57, v57
	v_add_f32_e32 v118, v77, v114
	v_cvt_pk_bf16_f32 v114, v66, v67
	v_cvt_pk_bf16_f32 v115, v68, v69
	s_waitcnt lgkmcnt(2)
	v_mfma_f32_32x32x16_bf16 v[98:113], v[192:195], v[146:149], v[98:113]
	s_waitcnt lgkmcnt(1)
	v_mfma_f32_32x32x16_bf16 v[82:97], v[158:161], v[142:145], v[82:97]
	ds_read_b128 v[66:69], v185 offset:6144
	ds_read_b128 v[188:191], v185 offset:6656
	v_add_f32_e32 v116, v78, v118
	v_add_f32_e32 v116, v79, v116
	v_add_f32_e32 v116, v80, v116
	v_exp_f32_e32 v58, v58
	v_exp_f32_e32 v59, v59
	v_exp_f32_e32 v60, v60
	v_exp_f32_e32 v61, v61
	v_add_f32_e32 v118, v81, v116
	v_cvt_pk_bf16_f32 v116, v70, v71
	v_cvt_pk_bf16_f32 v117, v72, v73
	s_nop 0
	v_exp_f32_e32 v62, v62
	v_exp_f32_e32 v63, v63
	v_exp_f32_e32 v64, v64
	v_exp_f32_e32 v65, v65
	v_cvt_pk_bf16_f32 v119, v76, v77
	v_add_f32_e32 v70, v118, v50
	v_add_f32_e32 v70, v51, v70
	v_add_f32_e32 v70, v52, v70
	v_add_f32_e32 v122, v53, v70
	v_cvt_pk_bf16_f32 v118, v74, v75
	s_waitcnt lgkmcnt(2)
	v_mfma_f32_32x32x16_bf16 v[98:113], v[196:199], v[142:145], v[98:113]
	s_waitcnt lgkmcnt(1)
	v_mfma_f32_32x32x16_bf16 v[82:97], v[66:69], v[138:141], v[82:97]
	ds_read_b128 v[70:73], v185 offset:8192
	ds_read_b128 v[74:77], v185 offset:8704
	v_add_f32_e32 v120, v122, v54
	v_add_f32_e32 v120, v55, v120
	v_add_f32_e32 v120, v56, v120
	v_add_f32_e32 v122, v57, v120
	v_cvt_pk_bf16_f32 v120, v78, v79
	v_cvt_pk_bf16_f32 v121, v80, v81
	s_nop 0
	v_add_f32_e32 v66, v58, v122
	v_add_f32_e32 v66, v59, v66
	v_add_f32_e32 v66, v60, v66
	v_add_f32_e32 v78, v61, v66
	v_cvt_pk_bf16_f32 v122, v50, v51
	v_cvt_pk_bf16_f32 v123, v52, v53
	s_waitcnt lgkmcnt(2)
	v_mfma_f32_32x32x16_bf16 v[98:113], v[188:191], v[138:141], v[98:113]
	s_waitcnt lgkmcnt(1)
	v_mfma_f32_32x32x16_bf16 v[82:97], v[70:73], v[134:137], v[82:97]
	ds_read_b128 v[50:53], v185 offset:10240
	ds_read_b128 v[66:69], v185 offset:10752
	v_add_f32_e32 v78, v62, v78
	v_add_f32_e32 v78, v63, v78
	v_add_f32_e32 v78, v64, v78
	v_add_f32_e32 v78, v65, v78
	v_cvt_pk_bf16_f32 v124, v54, v55
	v_cvt_pk_bf16_f32 v125, v56, v57
	v_cvt_pk_bf16_f32 v126, v58, v59
	v_cvt_pk_bf16_f32 v127, v60, v61
	s_waitcnt lgkmcnt(2)
	v_mfma_f32_32x32x16_bf16 v[98:113], v[74:77], v[134:137], v[98:113]
	s_waitcnt lgkmcnt(1)
	v_mfma_f32_32x32x16_bf16 v[82:97], v[50:53], v[130:133], v[82:97]
	v_cvt_pk_bf16_f32 v128, v62, v63
	v_cvt_pk_bf16_f32 v129, v64, v65
	s_waitcnt lgkmcnt(0)
; __device__ __forceinline__ float max3f(float a, float b, float c) { float r; asm("v_max3_f32 %0, %1, %2, %3" : "=v"(r) : "v"(a), "v"(b), "v"(c)); return r; }
; __device__ __forceinline__ void cmask(f32x16& p0, f32x16& p1, int jb, int qrel, int hi) {
;     const float NEG = -INFINITY; const int kb = 64 * jb + 4 * hi;
; #pragma unroll
;     for (int r = 0; r < 16; ++r) { const int kv = kb + (r & 3) + 8 * (r >> 2); if (kv > qrel) p0[r] = NEG; if (kv + 32 > qrel) p1[r] = NEG; }
; }
; __device__ __forceinline__ float rowmax(const f32x16& p0, const f32x16& p1) {
;     float a = max3f(p0[0], p0[1], p1[0]), b = max3f(p0[2], p0[3], p1[1]); a = max3f(a, p1[2], p1[3]);
; #pragma unroll
;     for (int r = 4; r < 16; r += 4) { a = max3f(a, p0[r], p0[r + 1]); b = max3f(b, p0[r + 2], p0[r + 3]); a = max3f(a, p1[r], p1[r + 1]); b = max3f(b, p1[r + 2], p1[r + 3]); }
;     const float m = fmaxf(a, b);
;     auto rr = __builtin_amdgcn_permlane32_swap(__float_as_uint(m), __float_as_uint(m), false, false);
;     return fmaxf(__uint_as_float(rr[0]), __uint_as_float(rr[1]));
; }
	v_mfma_f32_32x32x16_bf16 v[98:113], v[66:69], v[130:133], v[98:113]
	v_add_f32_e32 v158, v187, v78
	s_setprio 0
	v_or_b32_e32 v50, 0x60, v186
	v_or_b32_e32 v51, 64, v186
	v_cmp_le_i32_e32 vcc, v50, v182
	v_or_b32_e32 v52, 0x42, v186
	v_or_b32_e32 v53, 0x43, v186
	s_nop 4
	v_cndmask_b32_e32 v50, v206, v98, vcc
	v_cmp_lt_i32_e32 vcc, v51, v182
	v_or_b32_e32 v54, 0x48, v186
	v_or_b32_e32 v55, 0x49, v186
	v_cndmask_b32_e32 v67, v206, v83, vcc
	v_cmp_le_i32_e32 vcc, v51, v182
	v_or_b32_e32 v51, 0x61, v186
	v_or_b32_e32 v56, 0x4a, v186
	v_cndmask_b32_e32 v66, v206, v82, vcc
	v_cmp_le_i32_e32 vcc, v51, v182
	v_or_b32_e32 v57, 0x4b, v186
	v_or_b32_e32 v58, 0x50, v186
	v_cndmask_b32_e32 v51, v206, v99, vcc
	v_cmp_le_i32_e32 vcc, v52, v182
	v_or_b32_e32 v52, 0x62, v186
	v_or_b32_e32 v59, 0x51, v186
	v_cndmask_b32_e32 v68, v206, v84, vcc
	v_cmp_le_i32_e32 vcc, v52, v182
	v_or_b32_e32 v60, 0x52, v186
	v_or_b32_e32 v61, 0x53, v186
	v_cndmask_b32_e32 v52, v206, v100, vcc
	v_cmp_le_i32_e32 vcc, v53, v182
	v_or_b32_e32 v53, 0x63, v186
	v_or_b32_e32 v62, 0x58, v186
	v_cndmask_b32_e32 v69, v206, v85, vcc
	v_cmp_le_i32_e32 vcc, v53, v182
	v_or_b32_e32 v63, 0x59, v186
	v_max3_f32 v82, v66, v67, v50
	v_max3_f32 v83, v68, v69, v51
	v_or_b32_e32 v64, 0x5a, v186
	v_cndmask_b32_e32 v53, v206, v101, vcc
	v_cmp_le_i32_e32 vcc, v54, v182
	v_or_b32_e32 v54, 0x68, v186
	v_max3_f32 v82, v82, v52, v53
	v_or_b32_e32 v65, 0x5b, v186
	v_cndmask_b32_e32 v70, v206, v86, vcc
	v_cmp_le_i32_e32 vcc, v54, v182
	s_nop 1
	v_cndmask_b32_e32 v54, v206, v102, vcc
	v_cmp_le_i32_e32 vcc, v55, v182
	v_or_b32_e32 v55, 0x69, v186
	s_nop 0
	v_cndmask_b32_e32 v71, v206, v87, vcc
	v_cmp_le_i32_e32 vcc, v55, v182
	v_max3_f32 v82, v82, v70, v71
	s_nop 1
	v_cndmask_b32_e32 v55, v206, v103, vcc
	v_cmp_le_i32_e32 vcc, v56, v182
	v_or_b32_e32 v56, 0x6a, v186
	v_max3_f32 v82, v82, v54, v55
	s_nop 0
	v_cndmask_b32_e32 v72, v206, v88, vcc
	v_cmp_le_i32_e32 vcc, v56, v182
	s_nop 1
	v_cndmask_b32_e32 v56, v206, v104, vcc
	v_cmp_le_i32_e32 vcc, v57, v182
	v_or_b32_e32 v57, 0x6b, v186
	s_nop 0
	v_cndmask_b32_e32 v73, v206, v89, vcc
	v_cmp_le_i32_e32 vcc, v57, v182
	v_max3_f32 v83, v83, v72, v73
	s_nop 1
	v_cndmask_b32_e32 v57, v206, v105, vcc
	v_cmp_le_i32_e32 vcc, v58, v182
	v_or_b32_e32 v58, 0x70, v186
	v_max3_f32 v83, v83, v56, v57
	s_nop 0
	v_cndmask_b32_e32 v74, v206, v90, vcc
	v_cmp_le_i32_e32 vcc, v58, v182
	s_nop 1
	v_cndmask_b32_e32 v58, v206, v106, vcc
	v_cmp_le_i32_e32 vcc, v59, v182
	v_or_b32_e32 v59, 0x71, v186
	s_nop 0
	v_cndmask_b32_e32 v75, v206, v91, vcc
	v_cmp_le_i32_e32 vcc, v59, v182
	v_max3_f32 v82, v82, v74, v75
	s_nop 1
	v_cndmask_b32_e32 v59, v206, v107, vcc
	v_cmp_le_i32_e32 vcc, v60, v182
	v_or_b32_e32 v60, 0x72, v186
	v_max3_f32 v82, v82, v58, v59
	s_nop 0
	v_cndmask_b32_e32 v76, v206, v92, vcc
	v_cmp_le_i32_e32 vcc, v60, v182
	s_nop 1
	v_cndmask_b32_e32 v60, v206, v108, vcc
	v_cmp_le_i32_e32 vcc, v61, v182
	v_or_b32_e32 v61, 0x73, v186
	s_nop 0
	v_cndmask_b32_e32 v77, v206, v93, vcc
	v_cmp_le_i32_e32 vcc, v61, v182
	v_max3_f32 v83, v83, v76, v77
	s_nop 1
	v_cndmask_b32_e32 v61, v206, v109, vcc
	v_cmp_le_i32_e32 vcc, v62, v182
	v_or_b32_e32 v62, 0x78, v186
	v_max3_f32 v83, v83, v60, v61
	s_nop 0
	v_cndmask_b32_e32 v78, v206, v94, vcc
	v_cmp_le_i32_e32 vcc, v62, v182
	s_nop 1
	v_cndmask_b32_e32 v62, v206, v110, vcc
	v_cmp_le_i32_e32 vcc, v63, v182
	v_or_b32_e32 v63, 0x79, v186
	s_nop 0
	v_cndmask_b32_e32 v79, v206, v95, vcc
	v_cmp_le_i32_e32 vcc, v63, v182
	v_max3_f32 v82, v82, v78, v79
	s_nop 1
	v_cndmask_b32_e32 v63, v206, v111, vcc
	v_cmp_le_i32_e32 vcc, v64, v182
	v_or_b32_e32 v64, 0x7a, v186
	v_max3_f32 v82, v82, v62, v63
	s_nop 0
	v_cndmask_b32_e32 v80, v206, v96, vcc
	v_cmp_le_i32_e32 vcc, v64, v182
	v_max_f32_e32 v82, v82, v82
	s_nop 0
	v_cndmask_b32_e32 v64, v206, v112, vcc
	v_cmp_le_i32_e32 vcc, v65, v182
	v_or_b32_e32 v65, 0x7b, v186
	s_nop 0
	v_cndmask_b32_e32 v81, v206, v97, vcc
	v_cmp_le_i32_e32 vcc, v65, v182
	v_max3_f32 v83, v83, v80, v81
	s_nop 1
	v_cndmask_b32_e32 v65, v206, v113, vcc
	v_max3_f32 v83, v83, v64, v65
	s_nop 0
	v_max_f32_e32 v83, v83, v83
	v_max_f32_e32 v82, v82, v83
	v_mov_b32_e32 v83, v82
	s_nop 1
	v_permlane32_swap_b32_e32 v82, v83
	v_max_f32_e32 v83, v83, v83
	v_max_f32_e32 v82, v82, v82
	v_max_f32_e32 v82, v82, v83
	v_cmp_lt_f32_e32 vcc, s54, v82
	s_cmp_lg_u64 vcc, 0
	s_cselect_b64 s[42:43], -1, 0
	s_cbranch_vccnz .LBB0_1211

.LBB0_1136:
	s_mov_b32 m0, s73
	v_lshl_add_u64 v[82:83], v[156:157], 0, s[0:1]
	global_load_lds_dwordx4 v[82:83], off
	s_setprio 1
	ds_read_b128 v[98:101], v184
	ds_read_b128 v[188:191], v184 offset:512
	v_exp_f32_e32 v66, v66
	v_exp_f32_e32 v67, v67
	v_exp_f32_e32 v68, v68
	v_exp_f32_e32 v69, v69
	s_nop 0
	v_exp_f32_e32 v70, v70
	v_exp_f32_e32 v71, v71
	v_exp_f32_e32 v72, v72
	v_exp_f32_e32 v73, v73
	s_waitcnt lgkmcnt(1)
	v_mfma_f32_32x32x16_bf16 v[82:97], v[98:101], v[150:153], v[34:49]
	ds_read_b128 v[192:195], v184 offset:2048
	ds_read_b128 v[196:199], v184 offset:2560
	v_exp_f32_e32 v74, v74
	v_exp_f32_e32 v75, v75
	v_exp_f32_e32 v76, v76
	v_exp_f32_e32 v77, v77
	s_nop 0
	v_exp_f32_e32 v78, v78
	v_exp_f32_e32 v79, v79
	v_exp_f32_e32 v80, v80
	v_exp_f32_e32 v81, v81
	s_waitcnt lgkmcnt(2)
	v_mfma_f32_32x32x16_bf16 v[98:113], v[188:191], v[150:153], v[34:49]
	v_add_f32_e32 v114, 0, v66
	v_add_f32_e32 v114, v67, v114
	v_add_f32_e32 v114, v68, v114
	v_add_f32_e32 v114, v69, v114
	s_waitcnt lgkmcnt(1)
	v_mfma_f32_32x32x16_bf16 v[82:97], v[192:195], v[146:149], v[82:97]
	ds_read_b128 v[188:191], v184 offset:4096
	ds_read_b128 v[200:203], v184 offset:4608
	v_add_f32_e32 v114, v114, v70
	v_add_f32_e32 v114, v71, v114
	v_add_f32_e32 v114, v72, v114
	v_exp_f32_e32 v50, v50
	v_exp_f32_e32 v51, v51
	v_exp_f32_e32 v52, v52
	v_exp_f32_e32 v53, v53
	v_add_f32_e32 v114, v73, v114
	s_nop 0
	v_add_f32_e32 v114, v74, v114
	v_add_f32_e32 v114, v75, v114
	v_add_f32_e32 v114, v76, v114
	v_exp_f32_e32 v54, v54
	v_exp_f32_e32 v55, v55
	v_exp_f32_e32 v56, v56
	v_exp_f32_e32 v57, v57
	v_add_f32_e32 v118, v77, v114
	v_cvt_pk_bf16_f32 v114, v66, v67
	v_cvt_pk_bf16_f32 v115, v68, v69
	s_waitcnt lgkmcnt(2)
	v_mfma_f32_32x32x16_bf16 v[98:113], v[196:199], v[146:149], v[98:113]
	s_waitcnt lgkmcnt(1)
	v_mfma_f32_32x32x16_bf16 v[82:97], v[188:191], v[142:145], v[82:97]
	ds_read_b128 v[66:69], v184 offset:6144
	ds_read_b128 v[192:195], v184 offset:6656
	v_add_f32_e32 v116, v78, v118
	v_add_f32_e32 v116, v79, v116
	v_add_f32_e32 v116, v80, v116
	v_exp_f32_e32 v58, v58
	v_exp_f32_e32 v59, v59
	v_exp_f32_e32 v60, v60
	v_exp_f32_e32 v61, v61
	v_add_f32_e32 v118, v81, v116
	v_cvt_pk_bf16_f32 v116, v70, v71
	v_cvt_pk_bf16_f32 v117, v72, v73
	s_nop 0
	v_exp_f32_e32 v62, v62
	v_exp_f32_e32 v63, v63
	v_exp_f32_e32 v64, v64
	v_exp_f32_e32 v65, v65
	v_cvt_pk_bf16_f32 v119, v76, v77
	v_add_f32_e32 v70, v118, v50
	v_add_f32_e32 v70, v51, v70
	v_add_f32_e32 v70, v52, v70
	v_add_f32_e32 v122, v53, v70
	v_cvt_pk_bf16_f32 v118, v74, v75
	s_waitcnt lgkmcnt(2)
	v_mfma_f32_32x32x16_bf16 v[98:113], v[200:203], v[142:145], v[98:113]
	s_waitcnt lgkmcnt(1)
	v_mfma_f32_32x32x16_bf16 v[82:97], v[66:69], v[138:141], v[82:97]
	ds_read_b128 v[70:73], v184 offset:8192
	ds_read_b128 v[74:77], v184 offset:8704
	v_add_f32_e32 v120, v122, v54
	v_add_f32_e32 v120, v55, v120
	v_add_f32_e32 v120, v56, v120
	v_add_f32_e32 v122, v57, v120
	v_cvt_pk_bf16_f32 v120, v78, v79
	v_cvt_pk_bf16_f32 v121, v80, v81
	s_nop 0
	v_add_f32_e32 v66, v58, v122
	v_add_f32_e32 v66, v59, v66
	v_add_f32_e32 v66, v60, v66
	v_add_f32_e32 v78, v61, v66
	v_cvt_pk_bf16_f32 v122, v50, v51
	v_cvt_pk_bf16_f32 v123, v52, v53
	s_waitcnt lgkmcnt(2)
	v_mfma_f32_32x32x16_bf16 v[98:113], v[192:195], v[138:141], v[98:113]
	s_waitcnt lgkmcnt(1)
	v_mfma_f32_32x32x16_bf16 v[82:97], v[70:73], v[134:137], v[82:97]
	ds_read_b128 v[50:53], v184 offset:10240
	ds_read_b128 v[66:69], v184 offset:10752
	v_add_f32_e32 v78, v62, v78
	v_add_f32_e32 v78, v63, v78
	v_add_f32_e32 v78, v64, v78
	v_add_f32_e32 v78, v65, v78
	v_cvt_pk_bf16_f32 v124, v54, v55
	v_cvt_pk_bf16_f32 v125, v56, v57
	v_cvt_pk_bf16_f32 v126, v58, v59
	v_cvt_pk_bf16_f32 v127, v60, v61
	s_waitcnt lgkmcnt(2)
	v_mfma_f32_32x32x16_bf16 v[98:113], v[74:77], v[134:137], v[98:113]
	s_waitcnt lgkmcnt(1)
	v_mfma_f32_32x32x16_bf16 v[82:97], v[50:53], v[130:133], v[82:97]
	v_cvt_pk_bf16_f32 v128, v62, v63
	v_cvt_pk_bf16_f32 v129, v64, v65
	s_waitcnt lgkmcnt(0)
; __device__ __forceinline__ float max3f(float a, float b, float c) { float r; asm("v_max3_f32 %0, %1, %2, %3" : "=v"(r) : "v"(a), "v"(b), "v"(c)); return r; }
; __device__ __forceinline__ void cmask(f32x16& p0, f32x16& p1, int jb, int qrel, int hi) {
;     const float NEG = -INFINITY; const int kb = 64 * jb + 4 * hi;
; #pragma unroll
;     for (int r = 0; r < 16; ++r) { const int kv = kb + (r & 3) + 8 * (r >> 2); if (kv > qrel) p0[r] = NEG; if (kv + 32 > qrel) p1[r] = NEG; }
; }
; __device__ __forceinline__ float rowmax(const f32x16& p0, const f32x16& p1) {
;     float a = max3f(p0[0], p0[1], p1[0]), b = max3f(p0[2], p0[3], p1[1]); a = max3f(a, p1[2], p1[3]);
; #pragma unroll
;     for (int r = 4; r < 16; r += 4) { a = max3f(a, p0[r], p0[r + 1]); b = max3f(b, p0[r + 2], p0[r + 3]); a = max3f(a, p1[r], p1[r + 1]); b = max3f(b, p1[r + 2], p1[r + 3]); }
;     const float m = fmaxf(a, b);
;     auto rr = __builtin_amdgcn_permlane32_swap(__float_as_uint(m), __float_as_uint(m), false, false);
;     return fmaxf(__uint_as_float(rr[0]), __uint_as_float(rr[1]));
; }
	v_mfma_f32_32x32x16_bf16 v[98:113], v[66:69], v[130:133], v[98:113]
	v_add_f32_e32 v156, v158, v78
	s_setprio 0
	v_or_b32_e32 v50, 0xa0, v186
	v_or_b32_e32 v51, 0x80, v186
	v_cmp_le_i32_e32 vcc, v50, v182
	v_or_b32_e32 v52, 0x82, v186
	v_or_b32_e32 v53, 0x83, v186
	s_nop 4
	v_cndmask_b32_e32 v50, v206, v98, vcc
	v_cmp_lt_i32_e32 vcc, v51, v182
	v_or_b32_e32 v54, 0x88, v186
	v_or_b32_e32 v55, 0x89, v186
	v_cndmask_b32_e32 v67, v206, v83, vcc
	v_cmp_le_i32_e32 vcc, v51, v182
	v_or_b32_e32 v51, 0xa1, v186
	v_or_b32_e32 v56, 0x8a, v186
	v_cndmask_b32_e32 v66, v206, v82, vcc
	v_cmp_le_i32_e32 vcc, v51, v182
	v_or_b32_e32 v57, 0x8b, v186
	v_or_b32_e32 v58, 0x90, v186
	v_cndmask_b32_e32 v51, v206, v99, vcc
	v_cmp_le_i32_e32 vcc, v52, v182
	v_or_b32_e32 v52, 0xa2, v186
	v_or_b32_e32 v59, 0x91, v186
	v_cndmask_b32_e32 v68, v206, v84, vcc
	v_cmp_le_i32_e32 vcc, v52, v182
	v_or_b32_e32 v60, 0x92, v186
	v_or_b32_e32 v61, 0x93, v186
	v_cndmask_b32_e32 v52, v206, v100, vcc
	v_cmp_le_i32_e32 vcc, v53, v182
	v_or_b32_e32 v53, 0xa3, v186
	v_or_b32_e32 v62, 0x98, v186
	v_cndmask_b32_e32 v69, v206, v85, vcc
	v_cmp_le_i32_e32 vcc, v53, v182
	v_or_b32_e32 v63, 0x99, v186
	v_max3_f32 v82, v66, v67, v50
	v_max3_f32 v83, v68, v69, v51
	v_or_b32_e32 v64, 0x9a, v186
	v_cndmask_b32_e32 v53, v206, v101, vcc
	v_cmp_le_i32_e32 vcc, v54, v182
	v_or_b32_e32 v54, 0xa8, v186
	v_max3_f32 v82, v82, v52, v53
	v_or_b32_e32 v65, 0x9b, v186
	v_cndmask_b32_e32 v70, v206, v86, vcc
	v_cmp_le_i32_e32 vcc, v54, v182
	s_nop 1
	v_cndmask_b32_e32 v54, v206, v102, vcc
	v_cmp_le_i32_e32 vcc, v55, v182
	v_or_b32_e32 v55, 0xa9, v186
	s_nop 0
	v_cndmask_b32_e32 v71, v206, v87, vcc
	v_cmp_le_i32_e32 vcc, v55, v182
	v_max3_f32 v82, v82, v70, v71
	s_nop 1
	v_cndmask_b32_e32 v55, v206, v103, vcc
	v_cmp_le_i32_e32 vcc, v56, v182
	v_or_b32_e32 v56, 0xaa, v186
	v_max3_f32 v82, v82, v54, v55
	s_nop 0
	v_cndmask_b32_e32 v72, v206, v88, vcc
	v_cmp_le_i32_e32 vcc, v56, v182
	s_nop 1
	v_cndmask_b32_e32 v56, v206, v104, vcc
	v_cmp_le_i32_e32 vcc, v57, v182
	v_or_b32_e32 v57, 0xab, v186
	s_nop 0
	v_cndmask_b32_e32 v73, v206, v89, vcc
	v_cmp_le_i32_e32 vcc, v57, v182
	v_max3_f32 v83, v83, v72, v73
	s_nop 1
	v_cndmask_b32_e32 v57, v206, v105, vcc
	v_cmp_le_i32_e32 vcc, v58, v182
	v_or_b32_e32 v58, 0xb0, v186
	v_max3_f32 v83, v83, v56, v57
	s_nop 0
	v_cndmask_b32_e32 v74, v206, v90, vcc
	v_cmp_le_i32_e32 vcc, v58, v182
	s_nop 1
	v_cndmask_b32_e32 v58, v206, v106, vcc
	v_cmp_le_i32_e32 vcc, v59, v182
	v_or_b32_e32 v59, 0xb1, v186
	s_nop 0
	v_cndmask_b32_e32 v75, v206, v91, vcc
	v_cmp_le_i32_e32 vcc, v59, v182
	v_max3_f32 v82, v82, v74, v75
	s_nop 1
	v_cndmask_b32_e32 v59, v206, v107, vcc
	v_cmp_le_i32_e32 vcc, v60, v182
	v_or_b32_e32 v60, 0xb2, v186
	v_max3_f32 v82, v82, v58, v59
	s_nop 0
	v_cndmask_b32_e32 v76, v206, v92, vcc
	v_cmp_le_i32_e32 vcc, v60, v182
	s_nop 1
	v_cndmask_b32_e32 v60, v206, v108, vcc
	v_cmp_le_i32_e32 vcc, v61, v182
	v_or_b32_e32 v61, 0xb3, v186
	s_nop 0
	v_cndmask_b32_e32 v77, v206, v93, vcc
	v_cmp_le_i32_e32 vcc, v61, v182
	v_max3_f32 v83, v83, v76, v77
	s_nop 1
	v_cndmask_b32_e32 v61, v206, v109, vcc
	v_cmp_le_i32_e32 vcc, v62, v182
	v_or_b32_e32 v62, 0xb8, v186
	v_max3_f32 v83, v83, v60, v61
	s_nop 0
	v_cndmask_b32_e32 v78, v206, v94, vcc
	v_cmp_le_i32_e32 vcc, v62, v182
	s_nop 1
	v_cndmask_b32_e32 v62, v206, v110, vcc
	v_cmp_le_i32_e32 vcc, v63, v182
	v_or_b32_e32 v63, 0xb9, v186
	s_nop 0
	v_cndmask_b32_e32 v79, v206, v95, vcc
	v_cmp_le_i32_e32 vcc, v63, v182
	v_max3_f32 v82, v82, v78, v79
	s_nop 1
	v_cndmask_b32_e32 v63, v206, v111, vcc
	v_cmp_le_i32_e32 vcc, v64, v182
	v_or_b32_e32 v64, 0xba, v186
	v_max3_f32 v82, v82, v62, v63
	s_nop 0
	v_cndmask_b32_e32 v80, v206, v96, vcc
	v_cmp_le_i32_e32 vcc, v64, v182
	v_max_f32_e32 v82, v82, v82
	s_nop 0
	v_cndmask_b32_e32 v64, v206, v112, vcc
	v_cmp_le_i32_e32 vcc, v65, v182
	v_or_b32_e32 v65, 0xbb, v186
	s_nop 0
	v_cndmask_b32_e32 v81, v206, v97, vcc
	v_cmp_le_i32_e32 vcc, v65, v182
	v_max3_f32 v83, v83, v80, v81
	s_nop 1
	v_cndmask_b32_e32 v65, v206, v113, vcc
	v_max3_f32 v83, v83, v64, v65
	s_nop 0
	v_max_f32_e32 v83, v83, v83
	v_max_f32_e32 v82, v82, v83
	v_mov_b32_e32 v83, v82
	s_nop 1
	v_permlane32_swap_b32_e32 v82, v83
	v_max_f32_e32 v83, v83, v83
	v_max_f32_e32 v82, v82, v82
	v_max_f32_e32 v82, v82, v83
	v_cmp_lt_f32_e32 vcc, s54, v82
	s_cmp_lg_u64 vcc, 0
	s_cselect_b64 s[0:1], -1, 0
	s_cbranch_vccnz .LBB0_1214

; #define MLA_WAIT_BAR(N) asm volatile("s_waitcnt vmcnt(" #N ") lgkmcnt(0)\n\ts_barrier" ::: "memory")
; #define MLA_PIN(x) asm volatile("" : "+v"(x))
; #define MLA_LDK(kp, d0, h) (*(const __attribute__((address_space(3))) bf16x8*)((kp) + (d0) * 2048 + (h) * 512))
; #define MLA_MF(C, K, Q) C = __builtin_amdgcn_mfma_f32_32x32x16_bf16(K, Q, C, 0, 0, 0)
; template <int THRL, bool LATE> __device__ __forceinline__ void unit_stag(int b, int h, int qb, const unsigned short* Q, const unsigned short* KV, const unsigned short* KPE, unsigned short* O, char* shm, const int wave_) {
;     ...
;     glds16(ksrc, (unsigned)__builtin_amdgcn_readfirstlane(kdst)); if (lane < 32) glds16(psrc, (unsigned)__builtin_amdgcn_readfirstlane(pdst));
;     glds16(ksrc + (long)KVBLK * KVP, (unsigned)__builtin_amdgcn_readfirstlane(kdst + KSLOT)); if (lane < 32) glds16(psrc + (long)KVBLK * PEP, (unsigned)__builtin_amdgcn_readfirstlane(pdst + KSLOT)); glds16(vsrc, (unsigned)__builtin_amdgcn_readfirstlane(vdst));
;     glds16(ksrc + (long)2 * KVBLK * KVP, (unsigned)__builtin_amdgcn_readfirstlane(kdst + 2 * KSLOT)); if (lane < 32) glds16(psrc + (long)2 * KVBLK * PEP, (unsigned)__builtin_amdgcn_readfirstlane(pdst + 2 * KSLOT)); glds16(vsrc + (long)KVBLK * KVP, (unsigned)__builtin_amdgcn_readfirstlane(vdst + VSLOT));
;     float mhat = 0.f, l_reg = 0.f; f32x16 o[2]; o[0] = f32x16{}; o[1] = f32x16{}; f32x16 negm = f32x16{}; MLA_PIN(negm);
;     const int qrel = wid * QBLK + r32; bool resc = false;
;     f32x16 pA0, pA1, pB0, pB1; u32x4 pw0, pw1, pw2, pw3;
;     int s0 = 0, s1 = 1, s2 = 2;
;     MLA_WAIT_BAR(6);
;     { const lds_cptr kp = kp0;
;       pA0 = f32x16{}; pA1 = f32x16{};
; #pragma unroll
;       for (int d0 = 0; d0 < 6; ++d0) { const bf16x8 k0 = MLA_LDK(kp, d0, 0), k1 = MLA_LDK(kp, d0, 1); MLA_MF(pA0, k0, qr[d0]); MLA_MF(pA1, k1, qr[d0]); } }
;     { const float rm_ = rowmax(pA0, pA1); mhat = rm_;
; #pragma unroll
;       for (int r = 0; r < 16; ++r) { pA0[r] -= rm_; pA1[r] -= rm_; negm[r] = -mhat; }
;       MLA_PIN(negm); }
.LBB0_1148:
	s_or_b64 exec, exec, s[0:1]
	s_cmp_lg_u32 0, -1
	s_cselect_b32 s0, 0, 0
	s_add_i32 s0, s0, s42
	s_addk_i32 s0, 0x3000
	s_mov_b32 m0, s0
	v_lshl_add_u64 v[2:3], v[204:205], 0, s[12:13]
	global_load_lds_dwordx4 v[2:3], off
	s_and_saveexec_b64 s[0:1], s[2:3]
	s_cbranch_execz .LBB0_1150
	s_add_i32 s43, s70, 0x3000
	s_mov_b32 m0, s43
	v_lshl_add_u64 v[2:3], v[202:203], 0, s[14:15]
	global_load_lds_dwordx4 v[2:3], off
.LBB0_1150:
	s_or_b64 exec, exec, s[0:1]
	s_lshl_b32 s0, s68, 4
	v_lshrrev_b32_e32 v0, 2, v207
	v_and_or_b32 v0, s0, 48, v0
	s_ashr_i32 s0, s10, 3
	s_andn2_b32 s0, s0, 31
	s_ashr_i32 s1, s0, 31
	v_lshlrev_b32_e32 v208, 3, v34
	v_lshlrev_b32_e32 v0, 11, v0
	v_and_b32_e32 v35, 24, v208
	v_lshl_add_u64 v[2:3], s[36:37], 0, v[0:1]
	s_cmp_lg_u32 0, -1
	v_lshl_add_u64 v[2:3], s[0:1], 1, v[2:3]
	v_lshlrev_b32_e32 v0, 1, v35
	s_cselect_b32 s0, 0, 0
	v_lshl_add_u64 v[2:3], v[2:3], 0, v[0:1]
	s_add_i32 s0, s0, s42
	s_add_i32 s71, s0, 0x9000
	s_mov_b32 m0, s71
	v_lshl_add_u64 v[200:201], v[2:3], 0, s[16:17]
	global_load_lds_dwordx4 v[200:201], off
	s_addk_i32 s0, 0x6000
	s_mov_b32 m0, s0
	v_lshl_add_u64 v[2:3], v[204:205], 0, s[18:19]
	global_load_lds_dwordx4 v[2:3], off
	s_and_saveexec_b64 s[0:1], s[2:3]
	s_cbranch_execz .LBB0_1152
	s_add_i32 s43, s70, 0x6000
	s_mov_b32 m0, s43
	v_lshl_add_u64 v[2:3], v[202:203], 0, s[20:21]
	global_load_lds_dwordx4 v[2:3], off
.LBB0_1152:
	s_or_b64 exec, exec, s[0:1]
	s_cmp_lg_u32 0, -1
	v_lshlrev_b32_e32 v0, 10, v210
	v_lshlrev_b32_e32 v2, 4, v209
	s_cselect_b32 s0, 0, 0
	v_add3_u32 v213, 0, v0, v2
	s_add_i32 s0, s0, s42
	s_add_i32 s0, s0, 0xb000
	s_mov_b32 m0, s0
	v_lshl_add_u64 v[2:3], v[200:201], 0, s[12:13]
	global_load_lds_dwordx4 v[2:3], off
	v_mov_b32_e32 v2, v1
	v_mov_b32_e32 v3, v1
	v_mov_b32_e32 v4, v1
	v_mov_b32_e32 v5, v1
	v_mov_b32_e32 v6, v1
	v_mov_b32_e32 v7, v1
	v_mov_b32_e32 v8, v1
	v_mov_b32_e32 v9, v1
	v_mov_b32_e32 v10, v1
	v_mov_b32_e32 v11, v1
	v_mov_b32_e32 v12, v1
	v_mov_b32_e32 v13, v1
	v_mov_b32_e32 v14, v1
	v_mov_b32_e32 v15, v1
	v_mov_b32_e32 v0, v1
	v_mov_b64_e32 v[16:17], v[14:15]
	v_mov_b64_e32 v[14:15], v[12:13]
	v_mov_b64_e32 v[12:13], v[10:11]
	v_mov_b64_e32 v[10:11], v[8:9]
	v_mov_b64_e32 v[8:9], v[6:7]
	v_mov_b64_e32 v[6:7], v[4:5]
	v_mov_b64_e32 v[4:5], v[2:3]
	v_mov_b64_e32 v[2:3], v[0:1]
	s_waitcnt vmcnt(6) lgkmcnt(0)
	s_barrier
	ds_read_b128 v[2:5], v213
	ds_read_b128 v[6:9], v213 offset:512
	s_waitcnt vmcnt(5) lgkmcnt(1)
	v_mfma_f32_32x32x16_bf16 v[18:33], v[2:5], v[196:199], 0
	ds_read_b128 v[36:39], v213 offset:2048
	ds_read_b128 v[40:43], v213 offset:2560
	s_waitcnt lgkmcnt(2)
	v_mfma_f32_32x32x16_bf16 v[2:17], v[6:9], v[196:199], 0
	s_waitcnt vmcnt(4) lgkmcnt(1)
	v_mfma_f32_32x32x16_bf16 v[18:33], v[36:39], v[192:195], v[18:33]
	s_waitcnt lgkmcnt(0)
	v_mfma_f32_32x32x16_bf16 v[2:17], v[40:43], v[192:195], v[2:17]
	ds_read_b128 v[36:39], v213 offset:4096
	ds_read_b128 v[40:43], v213 offset:4608
	s_waitcnt vmcnt(3) lgkmcnt(1)
	v_mfma_f32_32x32x16_bf16 v[18:33], v[36:39], v[188:191], v[18:33]
	s_waitcnt lgkmcnt(0)
	v_mfma_f32_32x32x16_bf16 v[2:17], v[40:43], v[188:191], v[2:17]
	ds_read_b128 v[36:39], v213 offset:6144
	ds_read_b128 v[40:43], v213 offset:6656
	s_waitcnt vmcnt(2) lgkmcnt(1)
	v_mfma_f32_32x32x16_bf16 v[18:33], v[36:39], v[184:187], v[18:33]
	s_waitcnt lgkmcnt(0)
	v_mfma_f32_32x32x16_bf16 v[2:17], v[40:43], v[184:187], v[2:17]
	ds_read_b128 v[36:39], v213 offset:8192
	ds_read_b128 v[40:43], v213 offset:8704
	s_waitcnt vmcnt(1) lgkmcnt(1)
	v_mfma_f32_32x32x16_bf16 v[18:33], v[36:39], v[180:183], v[18:33]
	s_waitcnt lgkmcnt(0)
	v_mfma_f32_32x32x16_bf16 v[2:17], v[40:43], v[180:183], v[2:17]
	ds_read_b128 v[36:39], v213 offset:10240
	ds_read_b128 v[40:43], v213 offset:10752
	s_waitcnt vmcnt(0) lgkmcnt(1)
	v_mfma_f32_32x32x16_bf16 v[18:33], v[36:39], v[176:179], v[18:33]
	s_waitcnt lgkmcnt(0)
	v_mfma_f32_32x32x16_bf16 v[2:17], v[40:43], v[176:179], v[2:17]
	v_max3_f32 v0, v18, v19, v2
	v_max3_f32 v36, v20, v21, v3
	s_nop 0
	v_max3_f32 v0, v0, v4, v5
	v_max3_f32 v36, v36, v24, v25
	s_nop 0
	v_max3_f32 v0, v0, v22, v23
	v_max3_f32 v36, v36, v8, v9
	s_nop 0
	v_max3_f32 v0, v0, v6, v7
	v_max3_f32 v36, v36, v28, v29
	s_nop 0
	v_max3_f32 v0, v0, v26, v27
	v_max3_f32 v36, v36, v12, v13
	s_nop 0
	v_max3_f32 v0, v0, v10, v11
	v_max3_f32 v36, v36, v32, v33
	s_nop 0
	v_max3_f32 v0, v0, v30, v31
	v_max3_f32 v36, v36, v16, v17
	s_nop 0
	v_max3_f32 v0, v0, v14, v15
	v_max_f32_e32 v36, v36, v36
	v_max_f32_e32 v0, v0, v0
	v_max_f32_e32 v0, v0, v36
	v_mov_b32_e32 v36, v0
	s_nop 1
	v_permlane32_swap_b32_e32 v0, v36
	v_max_f32_e32 v36, v36, v36
	v_max_f32_e32 v0, v0, v0
	v_max_f32_e32 v0, v0, v36
	v_xor_b32_e32 v82, 0x80000000, v0
	v_mov_b32_e32 v83, v82
	v_mov_b32_e32 v84, v82
	v_mov_b32_e32 v85, v82
	v_mov_b32_e32 v86, v82
	v_mov_b32_e32 v87, v82
	v_mov_b32_e32 v88, v82
	v_mov_b32_e32 v89, v82
	v_mov_b32_e32 v90, v82
	v_mov_b32_e32 v91, v82
	v_mov_b32_e32 v92, v82
	v_mov_b32_e32 v93, v82
	v_mov_b32_e32 v94, v82
	v_mov_b32_e32 v95, v82
	v_mov_b32_e32 v96, v82
	v_mov_b32_e32 v97, v82
	s_waitcnt vmcnt(3) lgkmcnt(0)
	s_barrier
; #define MLA_PIN(x) asm volatile("" : "+v"(x))
; template <int THRL, bool LATE> __device__ __forceinline__ void unit_stag(int b, int h, int qb, const unsigned short* Q, const unsigned short* KV, const unsigned short* KPE, unsigned short* O, char* shm, const int wave_) {
;     ...
;     { const float rm_ = rowmax(pA0, pA1); mhat = rm_;
; #pragma unroll
;       for (int r = 0; r < 16; ++r) { pA0[r] -= rm_; pA1[r] -= rm_; negm[r] = -mhat; }
;       MLA_PIN(negm); }
	v_sub_f32_e32 v48, v2, v0
	v_sub_f32_e32 v2, v19, v0
	v_sub_f32_e32 v18, v18, v0
	v_sub_f32_e32 v49, v3, v0
	v_sub_f32_e32 v3, v20, v0
	v_sub_f32_e32 v50, v4, v0
	v_sub_f32_e32 v4, v21, v0
	v_sub_f32_e32 v51, v5, v0
	v_pk_add_f32 v[22:23], v[22:23], v[0:1] op_sel_hi:[1,0] neg_lo:[0,1] neg_hi:[0,1]
	v_pk_add_f32 v[6:7], v[6:7], v[0:1] op_sel_hi:[1,0] neg_lo:[0,1] neg_hi:[0,1]
	v_pk_add_f32 v[24:25], v[24:25], v[0:1] op_sel_hi:[1,0] neg_lo:[0,1] neg_hi:[0,1]
	v_pk_add_f32 v[8:9], v[8:9], v[0:1] op_sel_hi:[1,0] neg_lo:[0,1] neg_hi:[0,1]
	v_pk_add_f32 v[26:27], v[26:27], v[0:1] op_sel_hi:[1,0] neg_lo:[0,1] neg_hi:[0,1]
	v_pk_add_f32 v[10:11], v[10:11], v[0:1] op_sel_hi:[1,0] neg_lo:[0,1] neg_hi:[0,1]
	v_pk_add_f32 v[28:29], v[28:29], v[0:1] op_sel_hi:[1,0] neg_lo:[0,1] neg_hi:[0,1]
	v_pk_add_f32 v[12:13], v[12:13], v[0:1] op_sel_hi:[1,0] neg_lo:[0,1] neg_hi:[0,1]
	v_pk_add_f32 v[30:31], v[30:31], v[0:1] op_sel_hi:[1,0] neg_lo:[0,1] neg_hi:[0,1]
	v_pk_add_f32 v[14:15], v[14:15], v[0:1] op_sel_hi:[1,0] neg_lo:[0,1] neg_hi:[0,1]
	v_pk_add_f32 v[32:33], v[32:33], v[0:1] op_sel_hi:[1,0] neg_lo:[0,1] neg_hi:[0,1]
	v_pk_add_f32 v[16:17], v[16:17], v[0:1] op_sel_hi:[1,0] neg_lo:[0,1] neg_hi:[0,1]
	s_setprio 1
	v_exp_f32_e32 v19, v2
	v_exp_f32_e32 v20, v3
	v_exp_f32_e32 v21, v4
	ds_read_b128 v[2:5], v213 offset:12288
	ds_read_b128 v[36:39], v213 offset:12800
	v_exp_f32_e32 v18, v18
	s_nop 0
	v_exp_f32_e32 v22, v22
	v_exp_f32_e32 v23, v23
	v_exp_f32_e32 v24, v24
	v_exp_f32_e32 v25, v25
	s_waitcnt lgkmcnt(1)
	v_mfma_f32_32x32x16_bf16 v[98:113], v[2:5], v[196:199], v[82:97]
	ds_read_b128 v[40:43], v213 offset:14336
	ds_read_b128 v[44:47], v213 offset:14848
	v_exp_f32_e32 v26, v26
	v_exp_f32_e32 v27, v27
	v_exp_f32_e32 v28, v28
	v_exp_f32_e32 v29, v29
	s_waitcnt lgkmcnt(2)
	v_mfma_f32_32x32x16_bf16 v[114:129], v[36:39], v[196:199], v[82:97]
	v_exp_f32_e32 v30, v30
	v_exp_f32_e32 v31, v31
	v_exp_f32_e32 v32, v32
	v_exp_f32_e32 v33, v33
	s_nop 0
	v_add_f32_e32 v2, 0, v18
	v_add_f32_e32 v2, v19, v2
	v_add_f32_e32 v2, v20, v2
	v_add_f32_e32 v52, v21, v2
	s_waitcnt lgkmcnt(1)
	v_mfma_f32_32x32x16_bf16 v[98:113], v[40:43], v[192:195], v[98:113]
	v_exp_f32_e32 v2, v48
	v_exp_f32_e32 v3, v49
	v_exp_f32_e32 v4, v50
	v_exp_f32_e32 v5, v51
	ds_read_b128 v[36:39], v213 offset:16384
	ds_read_b128 v[48:51], v213 offset:16896
	v_add_f32_e32 v40, v52, v22
	v_add_f32_e32 v40, v23, v40
	v_add_f32_e32 v40, v24, v40
	v_add_f32_e32 v40, v25, v40
	s_waitcnt lgkmcnt(2)
	v_mfma_f32_32x32x16_bf16 v[114:129], v[44:47], v[192:195], v[114:129]
	v_add_f32_e32 v40, v26, v40
	v_add_f32_e32 v40, v27, v40
	v_add_f32_e32 v40, v28, v40
	v_exp_f32_e32 v6, v6
	v_exp_f32_e32 v7, v7
	v_exp_f32_e32 v8, v8
	v_exp_f32_e32 v9, v9
	v_add_f32_e32 v44, v29, v40
	v_cvt_pk_bf16_f32 v160, v18, v19
	v_cvt_pk_bf16_f32 v161, v20, v21
	s_waitcnt lgkmcnt(1)
	v_mfma_f32_32x32x16_bf16 v[98:113], v[36:39], v[188:191], v[98:113]
	ds_read_b128 v[18:21], v213 offset:18432
	ds_read_b128 v[40:43], v213 offset:18944
	v_add_f32_e32 v36, v30, v44
	v_add_f32_e32 v36, v31, v36
	v_add_f32_e32 v36, v32, v36
	v_exp_f32_e32 v10, v10
	v_exp_f32_e32 v11, v11
	v_exp_f32_e32 v12, v12
	v_exp_f32_e32 v13, v13
	v_add_f32_e32 v36, v33, v36
	v_cvt_pk_bf16_f32 v162, v22, v23
	v_cvt_pk_bf16_f32 v163, v24, v25
	s_waitcnt lgkmcnt(2)
	v_mfma_f32_32x32x16_bf16 v[114:129], v[48:51], v[188:191], v[114:129]
	v_exp_f32_e32 v14, v14
	v_exp_f32_e32 v15, v15
	v_exp_f32_e32 v16, v16
	v_exp_f32_e32 v17, v17
	v_cvt_pk_bf16_f32 v164, v26, v27
	v_add_f32_e32 v22, v36, v2
	v_add_f32_e32 v22, v3, v22
	v_add_f32_e32 v22, v4, v22
	v_add_f32_e32 v36, v5, v22
	v_cvt_pk_bf16_f32 v165, v28, v29
	s_waitcnt lgkmcnt(1)
	v_mfma_f32_32x32x16_bf16 v[98:113], v[18:21], v[184:187], v[98:113]
	ds_read_b128 v[22:25], v213 offset:20480
	ds_read_b128 v[26:29], v213 offset:20992
	v_add_f32_e32 v36, v36, v6
	v_add_f32_e32 v36, v7, v36
	v_add_f32_e32 v36, v8, v36
	v_add_f32_e32 v36, v9, v36
	v_cvt_pk_bf16_f32 v166, v30, v31
	v_cvt_pk_bf16_f32 v167, v32, v33
	s_waitcnt lgkmcnt(2)
	v_mfma_f32_32x32x16_bf16 v[114:129], v[40:43], v[184:187], v[114:129]
	v_add_f32_e32 v18, v10, v36
	v_add_f32_e32 v18, v11, v18
	v_add_f32_e32 v18, v12, v18
	v_add_f32_e32 v36, v13, v18
	v_cvt_pk_bf16_f32 v168, v2, v3
	v_cvt_pk_bf16_f32 v169, v4, v5
	s_waitcnt lgkmcnt(1)
	v_mfma_f32_32x32x16_bf16 v[98:113], v[22:25], v[180:183], v[98:113]
	ds_read_b128 v[18:21], v213 offset:22528
	ds_read_b128 v[30:33], v213 offset:23040
	v_add_f32_e32 v2, v14, v36
	v_add_f32_e32 v2, v15, v2
	v_add_f32_e32 v2, v16, v2
	v_add_f32_e32 v2, v17, v2
	v_cvt_pk_bf16_f32 v170, v6, v7
	v_cvt_pk_bf16_f32 v171, v8, v9
	s_waitcnt lgkmcnt(2)
	v_mfma_f32_32x32x16_bf16 v[114:129], v[26:29], v[180:183], v[114:129]
	v_cvt_pk_bf16_f32 v172, v10, v11
	v_cvt_pk_bf16_f32 v173, v12, v13
	s_waitcnt lgkmcnt(1)
	v_mfma_f32_32x32x16_bf16 v[98:113], v[18:21], v[176:179], v[98:113]
	v_cvt_pk_bf16_f32 v174, v14, v15
	v_cvt_pk_bf16_f32 v175, v16, v17
	s_waitcnt lgkmcnt(0)
	v_mfma_f32_32x32x16_bf16 v[114:129], v[30:33], v[176:179], v[114:129]
	s_setprio 0
	s_mov_b32 m0, s44
	v_lshl_add_u64 v[4:5], v[204:205], 0, s[22:23]
	global_load_lds_dwordx4 v[4:5], off
	s_and_saveexec_b64 s[0:1], s[2:3]
	s_cbranch_execz .LBB0_1154
	s_mov_b32 m0, s70
	v_lshl_add_u64 v[4:5], v[202:203], 0, s[26:27]
	global_load_lds_dwordx4 v[4:5], off
; __device__ __forceinline__ float max3f(float a, float b, float c) { float r; asm("v_max3_f32 %0, %1, %2, %3" : "=v"(r) : "v"(a), "v"(b), "v"(c)); return r; }
; __device__ __forceinline__ float rowmax(const f32x16& p0, const f32x16& p1) {
;     float a = max3f(p0[0], p0[1], p1[0]), b = max3f(p0[2], p0[3], p1[1]); a = max3f(a, p1[2], p1[3]);
; #pragma unroll
;     for (int r = 4; r < 16; r += 4) { a = max3f(a, p0[r], p0[r + 1]); b = max3f(b, p0[r + 2], p0[r + 3]); a = max3f(a, p1[r], p1[r + 1]); b = max3f(b, p1[r + 2], p1[r + 3]); }
;     const float m = fmaxf(a, b);
;     auto rr = __builtin_amdgcn_permlane32_swap(__float_as_uint(m), __float_as_uint(m), false, false);
;     return fmaxf(__uint_as_float(rr[0]), __uint_as_float(rr[1]));
; }
; __device__ __forceinline__ void pv(f32x16* o, int vb, bf16x8 pa0, bf16x8 pa1, bf16x8 pa2, bf16x8 pa3) {
; #pragma unroll
;     for (int d0 = 0; d0 < 2; ++d0) { s16x4 lo[4], hi[4];
; #pragma unroll
;         for (int ks = 0; ks < 4; ++ks) {
;             asm volatile("ds_read_b64_tr_b16 %0,%1 offset:%c2" : "=&v"(lo[ks]) : "v"(vb), "i"(d0 * 4096 + ks * 1024) : "memory");
;             asm volatile("ds_read_b64_tr_b16 %0,%1 offset:%c2" : "=&v"(hi[ks]) : "v"(vb), "i"(d0 * 4096 + ks * 1024 + 512) : "memory"); }
;         asm volatile("s_waitcnt lgkmcnt(0)" ::: "memory"); __builtin_amdgcn_sched_barrier(0);
;     ...
;         o[d0] = __builtin_amdgcn_mfma_f32_32x32x16_bf16(pa0, MLA_PK(0), o[d0], 0, 0, 0);
;         o[d0] = __builtin_amdgcn_mfma_f32_32x32x16_bf16(pa1, MLA_PK(1), o[d0], 0, 0, 0);
;         o[d0] = __builtin_amdgcn_mfma_f32_32x32x16_bf16(pa2, MLA_PK(2), o[d0], 0, 0, 0);
;         o[d0] = __builtin_amdgcn_mfma_f32_32x32x16_bf16(pa3, MLA_PK(3), o[d0], 0, 0, 0);
;     ...
;     }
; }
.LBB0_1154:
	s_or_b64 exec, exec, s[0:1]
	s_and_b32 s0, s10, 0x3fffffc0
	s_cmp_lg_u32 0, -1
	v_add_f32_e32 v216, 0, v2
	v_lshlrev_b32_e32 v2, 1, v34
	s_cselect_b32 s1, 0, 0
	v_and_b32_e32 v2, 32, v2
	v_lshlrev_b32_e32 v3, 4, v34
	s_add_i32 s10, s1, 0x9000
	s_lshl_b32 s0, s0, 2
	v_and_b32_e32 v3, 0xc0, v3
	v_add3_u32 v2, v2, s10, v35
	s_add_i32 s69, s0, 0
	v_lshlrev_b32_e32 v4, 8, v210
	s_add_i32 s0, s1, s42
	v_add3_u32 v211, v2, v3, v4
	s_add_i32 s0, s0, 0xd000
	s_mov_b32 m0, s0
	v_lshl_add_u64 v[2:3], v[200:201], 0, s[18:19]
	global_load_lds_dwordx4 v[2:3], off
	ds_read_b64_tr_b16 v[2:3],v211 offset:0
	ds_read_b64_tr_b16 v[4:5],v211 offset:512
	ds_read_b64_tr_b16 v[6:7],v211 offset:1024
	ds_read_b64_tr_b16 v[8:9],v211 offset:1536
	ds_read_b64_tr_b16 v[10:11],v211 offset:2048
	ds_read_b64_tr_b16 v[12:13],v211 offset:2560
	ds_read_b64_tr_b16 v[14:15],v211 offset:3072
	ds_read_b64_tr_b16 v[16:17],v211 offset:3584
	s_waitcnt lgkmcnt(0)
	s_add_i32 s69, s69, 0x11000
	v_mfma_f32_32x32x16_bf16 v[130:145], v[160:163], v[2:5], 0
	ds_read_b64_tr_b16 v[2:3],v211 offset:4096
	ds_read_b64_tr_b16 v[4:5],v211 offset:4608
	v_mfma_f32_32x32x16_bf16 v[130:145], v[164:167], v[6:9], v[130:145]
	ds_read_b64_tr_b16 v[6:7],v211 offset:5120
	ds_read_b64_tr_b16 v[8:9],v211 offset:5632
	v_mfma_f32_32x32x16_bf16 v[130:145], v[168:171], v[10:13], v[130:145]
	ds_read_b64_tr_b16 v[10:11],v211 offset:6144
	ds_read_b64_tr_b16 v[12:13],v211 offset:6656
	ds_read_b64_tr_b16 v[218:219],v211 offset:7168
	ds_read_b64_tr_b16 v[220:221],v211 offset:7680
	s_waitcnt lgkmcnt(0)
	v_mfma_f32_32x32x16_bf16 v[130:145], v[172:175], v[14:17], v[130:145]
	v_mfma_f32_32x32x16_bf16 v[146:161], v[160:163], v[2:5], 0
	v_max3_f32 v14, v98, v99, v114
	v_max3_f32 v15, v100, v101, v115
	s_mov_b64 s[0:1], -1
	v_max3_f32 v14, v14, v116, v117
	v_max3_f32 v15, v15, v104, v105
	v_mfma_f32_32x32x16_bf16 v[146:161], v[164:167], v[6:9], v[146:161]
	v_max3_f32 v14, v14, v102, v103
	v_max3_f32 v3, v15, v120, v121
	s_nop 0
	v_max3_f32 v2, v14, v118, v119
	v_max3_f32 v3, v3, v108, v109
	s_nop 0
	v_max3_f32 v2, v2, v106, v107
	v_mfma_f32_32x32x16_bf16 v[146:161], v[168:171], v[10:13], v[146:161]
	v_max3_f32 v2, v2, v122, v123
	v_max3_f32 v3, v3, v124, v125
	s_nop 0
	v_max3_f32 v2, v2, v110, v111
	v_max3_f32 v3, v3, v112, v113
	s_nop 0
	v_max3_f32 v2, v2, v126, v127
	v_max3_f32 v3, v3, v128, v129
	v_mfma_f32_32x32x16_bf16 v[146:161], v[172:175], v[218:221], v[146:161]
	v_max_f32_e32 v3, v3, v3
	v_max_f32_e32 v2, v2, v2
	v_max_f32_e32 v2, v2, v3
	v_mov_b32_e32 v3, v2
	s_nop 1
	v_permlane32_swap_b32_e32 v2, v3
	v_max_f32_e32 v3, v3, v3
	v_max_f32_e32 v2, v2, v2
	v_max_f32_e32 v164, v2, v3
	v_cmp_lt_f32_e32 vcc, s54, v164
	s_cbranch_vccnz .LBB0_1220
	s_and_b64 vcc, exec, s[0:1]
	s_cbranch_vccz .LBB0_1157
	v_mov_b64_e32 v[66:67], v[98:99]
	v_mov_b64_e32 v[18:19], v[146:147]
	v_mov_b64_e32 v[2:3], v[130:131]
	v_mov_b64_e32 v[50:51], v[114:115]
	v_mov_b64_e32 v[34:35], v[82:83]
	v_lshlrev_b32_e32 v214, 4, v210
	v_mov_b64_e32 v[68:69], v[100:101]
	v_mov_b64_e32 v[70:71], v[102:103]
	v_mov_b64_e32 v[72:73], v[104:105]
	v_mov_b64_e32 v[74:75], v[106:107]
	v_mov_b64_e32 v[76:77], v[108:109]
	v_mov_b64_e32 v[78:79], v[110:111]
	v_mov_b64_e32 v[80:81], v[112:113]
	v_mov_b64_e32 v[20:21], v[148:149]
	v_mov_b64_e32 v[22:23], v[150:151]
	v_mov_b64_e32 v[24:25], v[152:153]
	v_mov_b64_e32 v[26:27], v[154:155]
	v_mov_b64_e32 v[28:29], v[156:157]
	v_mov_b64_e32 v[30:31], v[158:159]
	v_mov_b64_e32 v[32:33], v[160:161]
	v_mov_b64_e32 v[4:5], v[132:133]
	v_mov_b64_e32 v[6:7], v[134:135]
	v_mov_b64_e32 v[8:9], v[136:137]
	v_mov_b64_e32 v[10:11], v[138:139]
	v_mov_b64_e32 v[12:13], v[140:141]
	v_mov_b64_e32 v[14:15], v[142:143]
	v_mov_b64_e32 v[16:17], v[144:145]
	v_mov_b64_e32 v[52:53], v[116:117]
	v_mov_b64_e32 v[54:55], v[118:119]
	v_mov_b64_e32 v[56:57], v[120:121]
	v_mov_b64_e32 v[58:59], v[122:123]
	v_mov_b64_e32 v[60:61], v[124:125]
	v_mov_b64_e32 v[62:63], v[126:127]
	v_mov_b64_e32 v[64:65], v[128:129]
	v_mov_b64_e32 v[36:37], v[84:85]
	v_mov_b64_e32 v[38:39], v[86:87]
	v_mov_b64_e32 v[40:41], v[88:89]
	v_mov_b64_e32 v[42:43], v[90:91]
	v_mov_b64_e32 v[44:45], v[92:93]
	v_mov_b64_e32 v[46:47], v[94:95]
	v_mov_b64_e32 v[48:49], v[96:97]
	v_mov_b32_e32 v215, v216
	v_mov_b32_e32 v212, v0

.LBB0_1158:
	s_mov_b32 s79, s45
	s_waitcnt vmcnt(3) lgkmcnt(0)
	s_barrier
	s_mul_i32 s72, s79, 0x3000
	s_mov_b32 s45, s42
	v_add_u32_e32 v133, s72, v213
	s_setprio 1
	ds_read_b128 v[82:85], v133
	ds_read_b128 v[116:119], v133 offset:512
	v_exp_f32_e32 v66, v66
	v_exp_f32_e32 v67, v67
	v_exp_f32_e32 v68, v68
	v_exp_f32_e32 v69, v69
	s_nop 0
	v_exp_f32_e32 v70, v70
	v_exp_f32_e32 v71, v71
	v_exp_f32_e32 v72, v72
	v_exp_f32_e32 v73, v73
	s_waitcnt lgkmcnt(1)
	v_mfma_f32_32x32x16_bf16 v[98:113], v[82:85], v[196:199], v[34:49]
	ds_read_b128 v[122:125], v133 offset:2048
	ds_read_b128 v[126:129], v133 offset:2560
	v_exp_f32_e32 v74, v74
	v_exp_f32_e32 v75, v75
	v_exp_f32_e32 v76, v76
	v_exp_f32_e32 v77, v77
	s_waitcnt lgkmcnt(2)
	v_mfma_f32_32x32x16_bf16 v[82:97], v[116:119], v[196:199], v[34:49]
	v_exp_f32_e32 v78, v78
	v_exp_f32_e32 v79, v79
	v_exp_f32_e32 v80, v80
	v_exp_f32_e32 v81, v81
	s_nop 0
	v_add_f32_e32 v0, 0, v66
	v_add_f32_e32 v0, v67, v0
	v_add_f32_e32 v0, v68, v0
	v_add_f32_e32 v0, v69, v0
	s_waitcnt lgkmcnt(1)
	v_mfma_f32_32x32x16_bf16 v[98:113], v[122:125], v[192:195], v[98:113]
	ds_read_b128 v[116:119], v133 offset:4096
	ds_read_b128 v[134:137], v133 offset:4608
	v_add_f32_e32 v0, v0, v70
	v_add_f32_e32 v0, v71, v0
	v_add_f32_e32 v0, v72, v0
	v_exp_f32_e32 v50, v50
	v_exp_f32_e32 v51, v51
	v_exp_f32_e32 v52, v52
	v_exp_f32_e32 v53, v53
	v_add_f32_e32 v0, v73, v0
	s_waitcnt lgkmcnt(2)
	v_mfma_f32_32x32x16_bf16 v[82:97], v[126:129], v[192:195], v[82:97]
	v_add_f32_e32 v0, v74, v0
	v_add_f32_e32 v0, v75, v0
	v_add_f32_e32 v0, v76, v0
	v_exp_f32_e32 v54, v54
	v_exp_f32_e32 v55, v55
	v_exp_f32_e32 v56, v56
	v_exp_f32_e32 v57, v57
	v_add_f32_e32 v0, v77, v0
	v_cvt_pk_bf16_f32 v160, v66, v67
	v_cvt_pk_bf16_f32 v161, v68, v69
	s_waitcnt lgkmcnt(1)
	v_mfma_f32_32x32x16_bf16 v[98:113], v[116:119], v[188:191], v[98:113]
	ds_read_b128 v[66:69], v133 offset:6144
	ds_read_b128 v[122:125], v133 offset:6656
	v_add_f32_e32 v0, v78, v0
	v_add_f32_e32 v0, v79, v0
	v_add_f32_e32 v0, v80, v0
	v_exp_f32_e32 v58, v58
	v_exp_f32_e32 v59, v59
	v_exp_f32_e32 v60, v60
	v_exp_f32_e32 v61, v61
	v_add_f32_e32 v0, v81, v0
	v_cvt_pk_bf16_f32 v162, v70, v71
	v_cvt_pk_bf16_f32 v163, v72, v73
	s_waitcnt lgkmcnt(2)
	v_mfma_f32_32x32x16_bf16 v[82:97], v[134:137], v[188:191], v[82:97]
	v_exp_f32_e32 v62, v62
	v_exp_f32_e32 v63, v63
	v_exp_f32_e32 v64, v64
	v_exp_f32_e32 v65, v65
	v_cvt_pk_bf16_f32 v164, v74, v75
	v_add_f32_e32 v0, v0, v50
	v_add_f32_e32 v0, v51, v0
	v_add_f32_e32 v0, v52, v0
	v_add_f32_e32 v0, v53, v0
	v_cvt_pk_bf16_f32 v165, v76, v77
	s_waitcnt lgkmcnt(1)
	v_mfma_f32_32x32x16_bf16 v[98:113], v[66:69], v[184:187], v[98:113]
	ds_read_b128 v[70:73], v133 offset:8192
	ds_read_b128 v[74:77], v133 offset:8704
	v_add_f32_e32 v0, v0, v54
	v_add_f32_e32 v0, v55, v0
	v_add_f32_e32 v0, v56, v0
	v_add_f32_e32 v0, v57, v0
	v_cvt_pk_bf16_f32 v166, v78, v79
	v_cvt_pk_bf16_f32 v167, v80, v81
	s_waitcnt lgkmcnt(2)
	v_mfma_f32_32x32x16_bf16 v[82:97], v[122:125], v[184:187], v[82:97]
	v_add_f32_e32 v0, v58, v0
	v_add_f32_e32 v0, v59, v0
	v_add_f32_e32 v0, v60, v0
	v_add_f32_e32 v0, v61, v0
	v_cvt_pk_bf16_f32 v168, v50, v51
	v_cvt_pk_bf16_f32 v169, v52, v53
	s_waitcnt lgkmcnt(1)
	v_mfma_f32_32x32x16_bf16 v[98:113], v[70:73], v[180:183], v[98:113]
	ds_read_b128 v[50:53], v133 offset:10240
	ds_read_b128 v[66:69], v133 offset:10752
	v_add_f32_e32 v0, v62, v0
	v_add_f32_e32 v0, v63, v0
	v_add_f32_e32 v0, v64, v0
	v_add_f32_e32 v0, v65, v0
	v_cvt_pk_bf16_f32 v170, v54, v55
	v_cvt_pk_bf16_f32 v171, v56, v57
	s_waitcnt lgkmcnt(2)
	v_mfma_f32_32x32x16_bf16 v[82:97], v[74:77], v[180:183], v[82:97]
	v_cvt_pk_bf16_f32 v172, v58, v59
	v_cvt_pk_bf16_f32 v173, v60, v61
	s_waitcnt lgkmcnt(1)
	v_mfma_f32_32x32x16_bf16 v[98:113], v[50:53], v[176:179], v[98:113]
	v_cvt_pk_bf16_f32 v174, v62, v63
	v_cvt_pk_bf16_f32 v175, v64, v65
	s_waitcnt lgkmcnt(0)
	v_mfma_f32_32x32x16_bf16 v[82:97], v[66:69], v[176:179], v[82:97]
	s_setprio 0
	v_lshl_add_u64 v[116:117], v[204:205], 0, s[0:1]
	s_mul_i32 s76, s42, 0x3000
	s_add_i32 s46, s76, s44
	s_mov_b32 m0, s46
	v_lshl_add_u64 v[50:51], v[116:117], 0, s[12:13]
	global_load_lds_dwordx4 v[50:51], off
	s_and_saveexec_b64 s[42:43], s[2:3]
	s_cbranch_execz .LBB0_1160
	s_add_i32 s73, s76, s70
	s_mov_b32 m0, s73
	v_lshl_add_u64 v[50:51], v[114:115], 0, s[30:31]
	global_load_lds_dwordx4 v[50:51], off
.LBB0_1160:
	s_or_b64 exec, exec, s[42:43]
	s_add_i32 s42, s81, 0x2000
	s_and_b32 s73, s42, 0x6000
	s_add_i32 s74, s73, s71
	s_mov_b32 m0, s74
	v_lshl_add_u64 v[118:119], v[200:201], 0, s[0:1]
	global_load_lds_dwordx4 v[118:119], off
	s_add_i32 s42, s81, 0xffffe000
	s_and_b32 s80, s42, 0x6000
	v_add_f32_e32 v121, v215, v0
	v_add_u32_e32 v0, s80, v211
	ds_read_b64_tr_b16 v[50:51],v0 offset:0
	ds_read_b64_tr_b16 v[52:53],v0 offset:512
	ds_read_b64_tr_b16 v[54:55],v0 offset:1024
	ds_read_b64_tr_b16 v[56:57],v0 offset:1536
	ds_read_b64_tr_b16 v[58:59],v0 offset:2048
	ds_read_b64_tr_b16 v[60:61],v0 offset:2560
	ds_read_b64_tr_b16 v[62:63],v0 offset:3072
	ds_read_b64_tr_b16 v[64:65],v0 offset:3584
	s_waitcnt lgkmcnt(0)
	s_nop 0
	v_mfma_f32_32x32x16_bf16 v[2:17], v[160:163], v[50:53], v[2:17]
	ds_read_b64_tr_b16 v[50:51],v0 offset:4096
	ds_read_b64_tr_b16 v[52:53],v0 offset:4608
	v_mfma_f32_32x32x16_bf16 v[2:17], v[164:167], v[54:57], v[2:17]
	ds_read_b64_tr_b16 v[54:55],v0 offset:5120
	ds_read_b64_tr_b16 v[56:57],v0 offset:5632
	v_mfma_f32_32x32x16_bf16 v[2:17], v[168:171], v[58:61], v[2:17]
	ds_read_b64_tr_b16 v[58:59],v0 offset:6144
	ds_read_b64_tr_b16 v[60:61],v0 offset:6656
	ds_read_b64_tr_b16 v[66:67],v0 offset:7168
	ds_read_b64_tr_b16 v[68:69],v0 offset:7680
	s_waitcnt lgkmcnt(0)
	v_mfma_f32_32x32x16_bf16 v[2:17], v[172:175], v[62:65], v[2:17]
	v_mfma_f32_32x32x16_bf16 v[18:33], v[160:163], v[50:53], v[18:33]
	v_max3_f32 v0, v98, v99, v82
	v_max3_f32 v62, v100, v101, v83
	s_nop 0
	v_max3_f32 v0, v0, v84, v85
	v_max3_f32 v50, v62, v104, v105
	s_nop 0
	v_max3_f32 v0, v0, v102, v103
	v_mfma_f32_32x32x16_bf16 v[18:33], v[164:167], v[54:57], v[18:33]
	v_max3_f32 v0, v0, v86, v87
	v_max3_f32 v50, v50, v88, v89
	s_nop 0
	v_max3_f32 v0, v0, v106, v107
	v_max3_f32 v50, v50, v108, v109
	s_nop 0
	v_max3_f32 v0, v0, v90, v91
	v_mfma_f32_32x32x16_bf16 v[18:33], v[168:171], v[58:61], v[18:33]
	v_max3_f32 v50, v50, v92, v93
	v_max3_f32 v0, v0, v110, v111
	s_nop 0
	v_max3_f32 v50, v50, v112, v113
	v_max3_f32 v0, v0, v94, v95
	s_nop 0
	v_max3_f32 v50, v50, v96, v97
	v_mfma_f32_32x32x16_bf16 v[18:33], v[172:175], v[66:69], v[18:33]
	v_max_f32_e32 v50, v50, v50
	v_max_f32_e32 v0, v0, v0
	v_max_f32_e32 v0, v0, v50
	v_mov_b32_e32 v50, v0
	s_nop 1
	v_permlane32_swap_b32_e32 v0, v50
	v_max_f32_e32 v50, v50, v50
	v_max_f32_e32 v0, v0, v0
	v_max_f32_e32 v0, v0, v50
	v_cmp_lt_f32_e32 vcc, s54, v0
	s_cbranch_vccnz .LBB0_1166
.LBB0_1161:
	s_waitcnt vmcnt(3) lgkmcnt(0)
	s_barrier
	s_mul_i32 s82, s47, 0x3000
	v_add_u32_e32 v132, s82, v213
	s_setprio 1
	ds_read_b128 v[50:53], v132
	ds_read_b128 v[122:125], v132 offset:512
	v_exp_f32_e32 v98, v98
	v_exp_f32_e32 v99, v99
	v_exp_f32_e32 v100, v100
	v_exp_f32_e32 v101, v101
	s_nop 0
	v_exp_f32_e32 v102, v102
	v_exp_f32_e32 v103, v103
	v_exp_f32_e32 v104, v104
	v_exp_f32_e32 v105, v105
	s_waitcnt lgkmcnt(1)
	v_mfma_f32_32x32x16_bf16 v[66:81], v[50:53], v[196:199], v[34:49]
	ds_read_b128 v[126:129], v132 offset:2048
	ds_read_b128 v[134:137], v132 offset:2560
	v_exp_f32_e32 v106, v106
	v_exp_f32_e32 v107, v107
	v_exp_f32_e32 v108, v108
	v_exp_f32_e32 v109, v109
	s_waitcnt lgkmcnt(2)
	v_mfma_f32_32x32x16_bf16 v[50:65], v[122:125], v[196:199], v[34:49]
	v_exp_f32_e32 v110, v110
	v_exp_f32_e32 v111, v111
	v_exp_f32_e32 v112, v112
	v_exp_f32_e32 v113, v113
	s_nop 0
	v_add_f32_e32 v0, 0, v98
	v_add_f32_e32 v0, v99, v0
	v_add_f32_e32 v0, v100, v0
	v_add_f32_e32 v0, v101, v0
	s_waitcnt lgkmcnt(1)
	v_mfma_f32_32x32x16_bf16 v[66:81], v[126:129], v[192:195], v[66:81]
	ds_read_b128 v[122:125], v132 offset:4096
	ds_read_b128 v[138:141], v132 offset:4608
	v_add_f32_e32 v0, v0, v102
	v_add_f32_e32 v0, v103, v0
	v_add_f32_e32 v0, v104, v0
	v_exp_f32_e32 v82, v82
	v_exp_f32_e32 v83, v83
	v_exp_f32_e32 v84, v84
	v_exp_f32_e32 v85, v85
	v_add_f32_e32 v0, v105, v0
	s_waitcnt lgkmcnt(2)
	v_mfma_f32_32x32x16_bf16 v[50:65], v[134:137], v[192:195], v[50:65]
	v_add_f32_e32 v0, v106, v0
	v_add_f32_e32 v0, v107, v0
	v_add_f32_e32 v0, v108, v0
	v_exp_f32_e32 v86, v86
	v_exp_f32_e32 v87, v87
	v_exp_f32_e32 v88, v88
	v_exp_f32_e32 v89, v89
	v_add_f32_e32 v0, v109, v0
	v_cvt_pk_bf16_f32 v160, v98, v99
	v_cvt_pk_bf16_f32 v161, v100, v101
	s_waitcnt lgkmcnt(1)
	v_mfma_f32_32x32x16_bf16 v[66:81], v[122:125], v[188:191], v[66:81]
	ds_read_b128 v[98:101], v132 offset:6144
	ds_read_b128 v[126:129], v132 offset:6656
	v_add_f32_e32 v0, v110, v0
	v_add_f32_e32 v0, v111, v0
	v_add_f32_e32 v0, v112, v0
	v_exp_f32_e32 v90, v90
	v_exp_f32_e32 v91, v91
	v_exp_f32_e32 v92, v92
	v_exp_f32_e32 v93, v93
	v_add_f32_e32 v0, v113, v0
	v_cvt_pk_bf16_f32 v162, v102, v103
	v_cvt_pk_bf16_f32 v163, v104, v105
	s_waitcnt lgkmcnt(2)
	v_mfma_f32_32x32x16_bf16 v[50:65], v[138:141], v[188:191], v[50:65]
	v_exp_f32_e32 v94, v94
	v_exp_f32_e32 v95, v95
	v_exp_f32_e32 v96, v96
	v_exp_f32_e32 v97, v97
	v_cvt_pk_bf16_f32 v164, v106, v107
	v_add_f32_e32 v0, v0, v82
	v_add_f32_e32 v0, v83, v0
	v_add_f32_e32 v0, v84, v0
	v_add_f32_e32 v0, v85, v0
	v_cvt_pk_bf16_f32 v165, v108, v109
	s_waitcnt lgkmcnt(1)
	v_mfma_f32_32x32x16_bf16 v[66:81], v[98:101], v[184:187], v[66:81]
	ds_read_b128 v[102:105], v132 offset:8192
	ds_read_b128 v[106:109], v132 offset:8704
	v_add_f32_e32 v0, v0, v86
	v_add_f32_e32 v0, v87, v0
	v_add_f32_e32 v0, v88, v0
	v_add_f32_e32 v0, v89, v0
	v_cvt_pk_bf16_f32 v166, v110, v111
	v_cvt_pk_bf16_f32 v167, v112, v113
	s_waitcnt lgkmcnt(2)
	v_mfma_f32_32x32x16_bf16 v[50:65], v[126:129], v[184:187], v[50:65]
	v_add_f32_e32 v0, v90, v0
	v_add_f32_e32 v0, v91, v0
	v_add_f32_e32 v0, v92, v0
	v_add_f32_e32 v0, v93, v0
	v_cvt_pk_bf16_f32 v168, v82, v83
	v_cvt_pk_bf16_f32 v169, v84, v85
	s_waitcnt lgkmcnt(1)
	v_mfma_f32_32x32x16_bf16 v[66:81], v[102:105], v[180:183], v[66:81]
	ds_read_b128 v[82:85], v132 offset:10240
	ds_read_b128 v[98:101], v132 offset:10752
	v_add_f32_e32 v0, v94, v0
	v_add_f32_e32 v0, v95, v0
	v_add_f32_e32 v0, v96, v0
	v_add_f32_e32 v0, v97, v0
	v_cvt_pk_bf16_f32 v170, v86, v87
	v_cvt_pk_bf16_f32 v171, v88, v89
	s_waitcnt lgkmcnt(2)
	v_mfma_f32_32x32x16_bf16 v[50:65], v[106:109], v[180:183], v[50:65]
	v_cvt_pk_bf16_f32 v172, v90, v91
	v_cvt_pk_bf16_f32 v173, v92, v93
	s_waitcnt lgkmcnt(1)
	v_mfma_f32_32x32x16_bf16 v[66:81], v[82:85], v[176:179], v[66:81]
	v_cvt_pk_bf16_f32 v174, v94, v95
	v_cvt_pk_bf16_f32 v175, v96, v97
	s_waitcnt lgkmcnt(0)
	v_mfma_f32_32x32x16_bf16 v[50:65], v[98:101], v[176:179], v[50:65]
	s_setprio 0
	s_add_i32 s42, s72, s44
	s_mov_b32 m0, s42
	v_lshl_add_u64 v[82:83], v[116:117], 0, s[18:19]
	global_load_lds_dwordx4 v[82:83], off
	s_and_saveexec_b64 s[42:43], s[2:3]
	s_cbranch_execz .LBB0_1163
	s_add_i32 s72, s72, s70
	s_mov_b32 m0, s72
	s_nop 0
	global_load_lds_dwordx4 v[114:115], off
.LBB0_1163:
	s_or_b64 exec, exec, s[42:43]
	s_add_i32 s72, s81, 0x4000
	s_and_b32 s77, s72, 0x6000
	s_add_i32 s42, s77, s71
	s_mov_b32 m0, s42
	v_lshl_add_u64 v[82:83], v[118:119], 0, s[12:13]
	global_load_lds_dwordx4 v[82:83], off
	s_and_b32 s42, s81, 0x6000
	v_add_f32_e32 v215, v121, v0
	v_add_u32_e32 v0, s42, v211
	ds_read_b64_tr_b16 v[82:83],v0 offset:0
	ds_read_b64_tr_b16 v[84:85],v0 offset:512
	ds_read_b64_tr_b16 v[86:87],v0 offset:1024
	ds_read_b64_tr_b16 v[88:89],v0 offset:1536
	ds_read_b64_tr_b16 v[90:91],v0 offset:2048
	ds_read_b64_tr_b16 v[92:93],v0 offset:2560
	ds_read_b64_tr_b16 v[94:95],v0 offset:3072
	ds_read_b64_tr_b16 v[96:97],v0 offset:3584
	s_waitcnt lgkmcnt(0)
	s_nop 0
	v_mfma_f32_32x32x16_bf16 v[2:17], v[160:163], v[82:85], v[2:17]
	ds_read_b64_tr_b16 v[82:83],v0 offset:4096
	ds_read_b64_tr_b16 v[84:85],v0 offset:4608
	v_mfma_f32_32x32x16_bf16 v[2:17], v[164:167], v[86:89], v[2:17]
	ds_read_b64_tr_b16 v[86:87],v0 offset:5120
	ds_read_b64_tr_b16 v[88:89],v0 offset:5632
	v_mfma_f32_32x32x16_bf16 v[2:17], v[168:171], v[90:93], v[2:17]
	ds_read_b64_tr_b16 v[90:91],v0 offset:6144
	ds_read_b64_tr_b16 v[92:93],v0 offset:6656
	ds_read_b64_tr_b16 v[98:99],v0 offset:7168
	ds_read_b64_tr_b16 v[100:101],v0 offset:7680
	s_waitcnt lgkmcnt(0)
	v_mfma_f32_32x32x16_bf16 v[2:17], v[172:175], v[94:97], v[2:17]
	v_mfma_f32_32x32x16_bf16 v[18:33], v[160:163], v[82:85], v[18:33]
	v_max3_f32 v0, v66, v67, v50
	v_max3_f32 v94, v68, v69, v51
	s_nop 0
	v_max3_f32 v0, v0, v52, v53
	v_max3_f32 v82, v94, v72, v73
	s_nop 0
	v_max3_f32 v0, v0, v70, v71
	v_mfma_f32_32x32x16_bf16 v[18:33], v[164:167], v[86:89], v[18:33]
	v_max3_f32 v0, v0, v54, v55
	v_max3_f32 v82, v82, v56, v57
	s_nop 0
	v_max3_f32 v0, v0, v74, v75
	v_max3_f32 v82, v82, v76, v77
	s_nop 0
	v_max3_f32 v0, v0, v58, v59
	v_mfma_f32_32x32x16_bf16 v[18:33], v[168:171], v[90:93], v[18:33]
	v_max3_f32 v82, v82, v60, v61
	v_max3_f32 v0, v0, v78, v79
	s_nop 0
	v_max3_f32 v82, v82, v80, v81
	v_max3_f32 v0, v0, v62, v63
	s_nop 0
	v_max3_f32 v82, v82, v64, v65
	v_mfma_f32_32x32x16_bf16 v[18:33], v[172:175], v[98:101], v[18:33]
	v_max_f32_e32 v82, v82, v82
	v_max_f32_e32 v0, v0, v0
	v_max_f32_e32 v0, v0, v82
	v_mov_b32_e32 v82, v0
	s_nop 1
	v_permlane32_swap_b32_e32 v0, v82
	v_max_f32_e32 v82, v82, v82
	v_max_f32_e32 v0, v0, v0
	v_max_f32_e32 v0, v0, v82
	v_cmp_lt_f32_e32 vcc, s54, v0
	s_cbranch_vccnz .LBB0_1169

.LBB0_1173:
	s_waitcnt vmcnt(3) lgkmcnt(0)
	s_barrier
	v_add_u32_e32 v130, s76, v213
	s_setprio 1
	ds_read_b128 v[98:101], v130
	ds_read_b128 v[114:117], v130 offset:512
	v_exp_f32_e32 v66, v66
	v_exp_f32_e32 v67, v67
	v_exp_f32_e32 v68, v68
	v_exp_f32_e32 v69, v69
	s_nop 0
	v_exp_f32_e32 v70, v70
	v_exp_f32_e32 v71, v71
	v_exp_f32_e32 v72, v72
	v_exp_f32_e32 v73, v73
	s_waitcnt lgkmcnt(1)
	v_mfma_f32_32x32x16_bf16 v[82:97], v[98:101], v[196:199], v[34:49]
	ds_read_b128 v[122:125], v130 offset:2048
	ds_read_b128 v[126:129], v130 offset:2560
	v_exp_f32_e32 v74, v74
	v_exp_f32_e32 v75, v75
	v_exp_f32_e32 v76, v76
	v_exp_f32_e32 v77, v77
	s_waitcnt lgkmcnt(2)
	v_mfma_f32_32x32x16_bf16 v[98:113], v[114:117], v[196:199], v[34:49]
	v_exp_f32_e32 v78, v78
	v_exp_f32_e32 v79, v79
	v_exp_f32_e32 v80, v80
	v_exp_f32_e32 v81, v81
	s_nop 0
	v_add_f32_e32 v0, 0, v66
	v_add_f32_e32 v0, v67, v0
	v_add_f32_e32 v0, v68, v0
	v_add_f32_e32 v0, v69, v0
	s_waitcnt lgkmcnt(1)
	v_mfma_f32_32x32x16_bf16 v[82:97], v[122:125], v[192:195], v[82:97]
	ds_read_b128 v[114:117], v130 offset:4096
	ds_read_b128 v[134:137], v130 offset:4608
	v_add_f32_e32 v0, v0, v70
	v_add_f32_e32 v0, v71, v0
	v_add_f32_e32 v0, v72, v0
	v_exp_f32_e32 v50, v50
	v_exp_f32_e32 v51, v51
	v_exp_f32_e32 v52, v52
	v_exp_f32_e32 v53, v53
	v_add_f32_e32 v0, v73, v0
	s_waitcnt lgkmcnt(2)
	v_mfma_f32_32x32x16_bf16 v[98:113], v[126:129], v[192:195], v[98:113]
	v_add_f32_e32 v0, v74, v0
	v_add_f32_e32 v0, v75, v0
	v_add_f32_e32 v0, v76, v0
	v_exp_f32_e32 v54, v54
	v_exp_f32_e32 v55, v55
	v_exp_f32_e32 v56, v56
	v_exp_f32_e32 v57, v57
	v_add_f32_e32 v0, v77, v0
	v_cvt_pk_bf16_f32 v160, v66, v67
	v_cvt_pk_bf16_f32 v161, v68, v69
	s_waitcnt lgkmcnt(1)
	v_mfma_f32_32x32x16_bf16 v[82:97], v[114:117], v[188:191], v[82:97]
	ds_read_b128 v[66:69], v130 offset:6144
	ds_read_b128 v[122:125], v130 offset:6656
	v_add_f32_e32 v0, v78, v0
	v_add_f32_e32 v0, v79, v0
	v_add_f32_e32 v0, v80, v0
	v_exp_f32_e32 v58, v58
	v_exp_f32_e32 v59, v59
	v_exp_f32_e32 v60, v60
	v_exp_f32_e32 v61, v61
	v_add_f32_e32 v0, v81, v0
	v_cvt_pk_bf16_f32 v162, v70, v71
	v_cvt_pk_bf16_f32 v163, v72, v73
	s_waitcnt lgkmcnt(2)
	v_mfma_f32_32x32x16_bf16 v[98:113], v[134:137], v[188:191], v[98:113]
	v_exp_f32_e32 v62, v62
	v_exp_f32_e32 v63, v63
	v_exp_f32_e32 v64, v64
	v_exp_f32_e32 v65, v65
	v_cvt_pk_bf16_f32 v164, v74, v75
	v_add_f32_e32 v0, v0, v50
	v_add_f32_e32 v0, v51, v0
	v_add_f32_e32 v0, v52, v0
	v_add_f32_e32 v0, v53, v0
	v_cvt_pk_bf16_f32 v165, v76, v77
	s_waitcnt lgkmcnt(1)
	v_mfma_f32_32x32x16_bf16 v[82:97], v[66:69], v[184:187], v[82:97]
	ds_read_b128 v[70:73], v130 offset:8192
	ds_read_b128 v[74:77], v130 offset:8704
	v_add_f32_e32 v0, v0, v54
	v_add_f32_e32 v0, v55, v0
	v_add_f32_e32 v0, v56, v0
	v_add_f32_e32 v0, v57, v0
	v_cvt_pk_bf16_f32 v166, v78, v79
	v_cvt_pk_bf16_f32 v167, v80, v81
	s_waitcnt lgkmcnt(2)
	v_mfma_f32_32x32x16_bf16 v[98:113], v[122:125], v[184:187], v[98:113]
	v_add_f32_e32 v0, v58, v0
	v_add_f32_e32 v0, v59, v0
	v_add_f32_e32 v0, v60, v0
	v_add_f32_e32 v0, v61, v0
	v_cvt_pk_bf16_f32 v168, v50, v51
	v_cvt_pk_bf16_f32 v169, v52, v53
	s_waitcnt lgkmcnt(1)
	v_mfma_f32_32x32x16_bf16 v[82:97], v[70:73], v[180:183], v[82:97]
	ds_read_b128 v[50:53], v130 offset:10240
	ds_read_b128 v[66:69], v130 offset:10752
	v_add_f32_e32 v0, v62, v0
	v_add_f32_e32 v0, v63, v0
	v_add_f32_e32 v0, v64, v0
	v_add_f32_e32 v0, v65, v0
	v_cvt_pk_bf16_f32 v170, v54, v55
	v_cvt_pk_bf16_f32 v171, v56, v57
	s_waitcnt lgkmcnt(2)
	v_mfma_f32_32x32x16_bf16 v[98:113], v[74:77], v[180:183], v[98:113]
	v_cvt_pk_bf16_f32 v172, v58, v59
	v_cvt_pk_bf16_f32 v173, v60, v61
	s_waitcnt lgkmcnt(1)
	v_mfma_f32_32x32x16_bf16 v[82:97], v[50:53], v[176:179], v[82:97]
	v_cvt_pk_bf16_f32 v174, v62, v63
	v_cvt_pk_bf16_f32 v175, v64, v65
	s_waitcnt lgkmcnt(0)
	v_mfma_f32_32x32x16_bf16 v[98:113], v[66:69], v[176:179], v[98:113]
	s_setprio 0
	s_add_i32 s10, s81, 5
	s_lshl_b64 s[42:43], s[10:11], 17
	s_add_i32 s44, s82, s44
	s_mov_b32 m0, s44
	v_lshl_add_u64 v[50:51], v[204:205], 0, s[42:43]
	global_load_lds_dwordx4 v[50:51], off
	s_and_saveexec_b64 s[44:45], s[2:3]
	s_cbranch_execz .LBB0_1175
	s_lshl_b64 s[78:79], s[10:11], 12
	s_add_i32 s47, s82, s70
	s_mov_b32 m0, s47
	v_lshl_add_u64 v[50:51], v[202:203], 0, s[78:79]
	global_load_lds_dwordx4 v[50:51], off

.LBB0_1176:
	s_waitcnt vmcnt(3) lgkmcnt(0)
	s_barrier
	s_setprio 1
	ds_read_b128 v[98:101], v133
	ds_read_b128 v[136:139], v133 offset:512
	v_exp_f32_e32 v66, v66
	v_exp_f32_e32 v67, v67
	v_exp_f32_e32 v68, v68
	v_exp_f32_e32 v69, v69
	s_nop 0
	v_exp_f32_e32 v70, v70
	v_exp_f32_e32 v71, v71
	v_exp_f32_e32 v72, v72
	v_exp_f32_e32 v73, v73
	s_waitcnt lgkmcnt(1)
	v_mfma_f32_32x32x16_bf16 v[82:97], v[98:101], v[196:199], v[34:49]
	ds_read_b128 v[140:143], v133 offset:2048
	ds_read_b128 v[144:147], v133 offset:2560
	v_exp_f32_e32 v74, v74
	v_exp_f32_e32 v75, v75
	v_exp_f32_e32 v76, v76
	v_exp_f32_e32 v77, v77
	s_waitcnt lgkmcnt(2)
	v_mfma_f32_32x32x16_bf16 v[98:113], v[136:139], v[196:199], v[34:49]
	v_exp_f32_e32 v78, v78
	v_exp_f32_e32 v79, v79
	v_exp_f32_e32 v80, v80
	v_exp_f32_e32 v81, v81
	s_nop 0
	v_add_f32_e32 v0, 0, v66
	v_add_f32_e32 v0, v67, v0
	v_add_f32_e32 v0, v68, v0
	v_add_f32_e32 v0, v69, v0
	s_waitcnt lgkmcnt(1)
	v_mfma_f32_32x32x16_bf16 v[82:97], v[140:143], v[192:195], v[82:97]
	ds_read_b128 v[136:139], v133 offset:4096
	ds_read_b128 v[148:151], v133 offset:4608
	v_add_f32_e32 v0, v0, v70
	v_add_f32_e32 v0, v71, v0
	v_add_f32_e32 v0, v72, v0
	v_exp_f32_e32 v50, v50
	v_exp_f32_e32 v51, v51
	v_exp_f32_e32 v52, v52
	v_exp_f32_e32 v53, v53
	v_add_f32_e32 v0, v73, v0
	s_waitcnt lgkmcnt(2)
	v_mfma_f32_32x32x16_bf16 v[98:113], v[144:147], v[192:195], v[98:113]
	v_add_f32_e32 v0, v74, v0
	v_add_f32_e32 v0, v75, v0
	v_add_f32_e32 v0, v76, v0
	v_exp_f32_e32 v54, v54
	v_exp_f32_e32 v55, v55
	v_exp_f32_e32 v56, v56
	v_exp_f32_e32 v57, v57
	v_add_f32_e32 v0, v77, v0
	v_cvt_pk_bf16_f32 v160, v66, v67
	v_cvt_pk_bf16_f32 v161, v68, v69
	s_waitcnt lgkmcnt(1)
	v_mfma_f32_32x32x16_bf16 v[82:97], v[136:139], v[188:191], v[82:97]
	ds_read_b128 v[66:69], v133 offset:6144
	ds_read_b128 v[140:143], v133 offset:6656
	v_add_f32_e32 v0, v78, v0
	v_add_f32_e32 v0, v79, v0
	v_add_f32_e32 v0, v80, v0
	v_exp_f32_e32 v58, v58
	v_exp_f32_e32 v59, v59
	v_exp_f32_e32 v60, v60
	v_exp_f32_e32 v61, v61
	v_add_f32_e32 v0, v81, v0
	v_cvt_pk_bf16_f32 v162, v70, v71
	v_cvt_pk_bf16_f32 v163, v72, v73
	s_waitcnt lgkmcnt(2)
	v_mfma_f32_32x32x16_bf16 v[98:113], v[148:151], v[188:191], v[98:113]
	v_exp_f32_e32 v62, v62
	v_exp_f32_e32 v63, v63
	v_exp_f32_e32 v64, v64
	v_exp_f32_e32 v65, v65
	v_cvt_pk_bf16_f32 v164, v74, v75
	v_add_f32_e32 v0, v0, v50
	v_add_f32_e32 v0, v51, v0
	v_add_f32_e32 v0, v52, v0
	v_add_f32_e32 v0, v53, v0
	v_cvt_pk_bf16_f32 v165, v76, v77
	s_waitcnt lgkmcnt(1)
	v_mfma_f32_32x32x16_bf16 v[82:97], v[66:69], v[184:187], v[82:97]
	ds_read_b128 v[70:73], v133 offset:8192
	ds_read_b128 v[74:77], v133 offset:8704
	v_add_f32_e32 v0, v0, v54
	v_add_f32_e32 v0, v55, v0
	v_add_f32_e32 v0, v56, v0
	v_add_f32_e32 v0, v57, v0
	v_cvt_pk_bf16_f32 v166, v78, v79
	v_cvt_pk_bf16_f32 v167, v80, v81
	s_waitcnt lgkmcnt(2)
	v_mfma_f32_32x32x16_bf16 v[98:113], v[140:143], v[184:187], v[98:113]
	v_add_f32_e32 v0, v58, v0
	v_add_f32_e32 v0, v59, v0
	v_add_f32_e32 v0, v60, v0
	v_add_f32_e32 v0, v61, v0
	v_cvt_pk_bf16_f32 v168, v50, v51
	v_cvt_pk_bf16_f32 v169, v52, v53
	s_waitcnt lgkmcnt(1)
	v_mfma_f32_32x32x16_bf16 v[82:97], v[70:73], v[180:183], v[82:97]
	ds_read_b128 v[50:53], v133 offset:10240
	ds_read_b128 v[66:69], v133 offset:10752
	v_add_f32_e32 v0, v62, v0
	v_add_f32_e32 v0, v63, v0
	v_add_f32_e32 v0, v64, v0
	v_add_f32_e32 v0, v65, v0
	v_cvt_pk_bf16_f32 v170, v54, v55
	v_cvt_pk_bf16_f32 v171, v56, v57
	s_waitcnt lgkmcnt(2)
	v_mfma_f32_32x32x16_bf16 v[98:113], v[74:77], v[180:183], v[98:113]
	v_cvt_pk_bf16_f32 v172, v58, v59
	v_cvt_pk_bf16_f32 v173, v60, v61
	s_waitcnt lgkmcnt(1)
	v_mfma_f32_32x32x16_bf16 v[82:97], v[50:53], v[176:179], v[82:97]
	v_cvt_pk_bf16_f32 v174, v62, v63
	v_cvt_pk_bf16_f32 v175, v64, v65
	s_waitcnt lgkmcnt(0)
	v_mfma_f32_32x32x16_bf16 v[98:113], v[66:69], v[176:179], v[98:113]
	s_setprio 0
	s_add_i32 s44, s81, 6
	s_mov_b32 s45, s11
	s_lshl_b64 s[0:1], s[44:45], 17
	s_mov_b32 m0, s46
	v_lshl_add_u64 v[50:51], v[204:205], 0, s[0:1]
	global_load_lds_dwordx4 v[50:51], off
	s_and_saveexec_b64 s[46:47], s[2:3]
	s_cbranch_execz .LBB0_1178
	s_lshl_b64 s[44:45], s[44:45], 12
	s_add_i32 s70, s76, s70
	s_mov_b32 m0, s70
	v_lshl_add_u64 v[50:51], v[202:203], 0, s[44:45]
	global_load_lds_dwordx4 v[50:51], off
; __device__ __forceinline__ float max3f(float a, float b, float c) { float r; asm("v_max3_f32 %0, %1, %2, %3" : "=v"(r) : "v"(a), "v"(b), "v"(c)); return r; }
; __device__ __forceinline__ void cmask(f32x16& p0, f32x16& p1, int jb, int qrel, int hi) {
;     const float NEG = -INFINITY; const int kb = 64 * jb + 4 * hi;
; #pragma unroll
;     for (int r = 0; r < 16; ++r) { const int kv = kb + (r & 3) + 8 * (r >> 2); if (kv > qrel) p0[r] = NEG; if (kv + 32 > qrel) p1[r] = NEG; }
; }
; __device__ __forceinline__ float rowmax(const f32x16& p0, const f32x16& p1) {
;     float a = max3f(p0[0], p0[1], p1[0]), b = max3f(p0[2], p0[3], p1[1]); a = max3f(a, p1[2], p1[3]);
; #pragma unroll
;     for (int r = 4; r < 16; r += 4) { a = max3f(a, p0[r], p0[r + 1]); b = max3f(b, p0[r + 2], p0[r + 3]); a = max3f(a, p1[r], p1[r + 1]); b = max3f(b, p1[r + 2], p1[r + 3]); }
;     const float m = fmaxf(a, b);
;     auto rr = __builtin_amdgcn_permlane32_swap(__float_as_uint(m), __float_as_uint(m), false, false);
;     return fmaxf(__uint_as_float(rr[0]), __uint_as_float(rr[1]));
; }
; __device__ __forceinline__ void pv(f32x16* o, int vb, bf16x8 pa0, bf16x8 pa1, bf16x8 pa2, bf16x8 pa3) {
; #pragma unroll
;     for (int d0 = 0; d0 < 2; ++d0) { s16x4 lo[4], hi[4];
; #pragma unroll
;         for (int ks = 0; ks < 4; ++ks) {
;             asm volatile("ds_read_b64_tr_b16 %0,%1 offset:%c2" : "=&v"(lo[ks]) : "v"(vb), "i"(d0 * 4096 + ks * 1024) : "memory");
;             asm volatile("ds_read_b64_tr_b16 %0,%1 offset:%c2" : "=&v"(hi[ks]) : "v"(vb), "i"(d0 * 4096 + ks * 1024 + 512) : "memory"); }
;         asm volatile("s_waitcnt lgkmcnt(0)" ::: "memory"); __builtin_amdgcn_sched_barrier(0);
;     ...
;         o[d0] = __builtin_amdgcn_mfma_f32_32x32x16_bf16(pa0, MLA_PK(0), o[d0], 0, 0, 0);
;         o[d0] = __builtin_amdgcn_mfma_f32_32x32x16_bf16(pa1, MLA_PK(1), o[d0], 0, 0, 0);
;         o[d0] = __builtin_amdgcn_mfma_f32_32x32x16_bf16(pa2, MLA_PK(2), o[d0], 0, 0, 0);
;         o[d0] = __builtin_amdgcn_mfma_f32_32x32x16_bf16(pa3, MLA_PK(3), o[d0], 0, 0, 0);
;     ...
;     }
; }
.LBB0_1178:
	s_or_b64 exec, exec, s[46:47]
	s_lshl_b32 s10, s10, 13
	s_and_b32 s10, s10, 0x6000
	s_add_i32 s10, s10, s71
	s_mov_b32 m0, s10
	v_lshl_add_u64 v[50:51], v[200:201], 0, s[42:43]
	global_load_lds_dwordx4 v[50:51], off
	v_add_f32_e32 v133, v134, v0
	v_add_u32_e32 v0, s77, v211
	ds_read_b64_tr_b16 v[50:51],v0 offset:0
	ds_read_b64_tr_b16 v[52:53],v0 offset:512
	ds_read_b64_tr_b16 v[54:55],v0 offset:1024
	ds_read_b64_tr_b16 v[56:57],v0 offset:1536
	ds_read_b64_tr_b16 v[58:59],v0 offset:2048
	ds_read_b64_tr_b16 v[60:61],v0 offset:2560
	ds_read_b64_tr_b16 v[62:63],v0 offset:3072
	ds_read_b64_tr_b16 v[64:65],v0 offset:3584
	s_waitcnt lgkmcnt(0)
	s_nop 0
	v_mfma_f32_32x32x16_bf16 v[2:17], v[160:163], v[50:53], v[2:17]
	ds_read_b64_tr_b16 v[52:53],v0 offset:4096
	v_mfma_f32_32x32x16_bf16 v[2:17], v[164:167], v[54:57], v[2:17]
	ds_read_b64_tr_b16 v[54:55],v0 offset:4608
	ds_read_b64_tr_b16 v[56:57],v0 offset:5120
	v_mfma_f32_32x32x16_bf16 v[2:17], v[168:171], v[58:61], v[2:17]
	ds_read_b64_tr_b16 v[58:59],v0 offset:5632
	ds_read_b64_tr_b16 v[70:71],v0 offset:6144
	ds_read_b64_tr_b16 v[72:73],v0 offset:6656
	ds_read_b64_tr_b16 v[74:75],v0 offset:7168
	ds_read_b64_tr_b16 v[76:77],v0 offset:7680
	s_waitcnt lgkmcnt(0)
	v_mfma_f32_32x32x16_bf16 v[2:17], v[172:175], v[62:65], v[2:17]
	v_mfma_f32_32x32x16_bf16 v[18:33], v[160:163], v[52:55], v[18:33]
	v_or_b32_e32 v50, 0x60, v129
	v_or_b32_e32 v0, 64, v129
	v_cmp_le_i32_e32 vcc, v50, v131
	s_nop 1
	v_cndmask_b32_e32 v50, v206, v98, vcc
	v_cmp_lt_i32_e32 vcc, v0, v131
	v_mfma_f32_32x32x16_bf16 v[18:33], v[164:167], v[56:59], v[18:33]
	s_nop 0
	v_cndmask_b32_e32 v67, v206, v83, vcc
	v_cmp_le_i32_e32 vcc, v0, v131
	v_or_b32_e32 v0, 0x61, v129
	s_nop 0
	v_cndmask_b32_e32 v66, v206, v82, vcc
	v_cmp_le_i32_e32 vcc, v0, v131
	v_or_b32_e32 v0, 0x42, v129
	v_mfma_f32_32x32x16_bf16 v[18:33], v[168:171], v[70:73], v[18:33]
	v_cndmask_b32_e32 v51, v206, v99, vcc
	v_cmp_le_i32_e32 vcc, v0, v131
	v_or_b32_e32 v0, 0x62, v129
	s_nop 0
	v_cndmask_b32_e32 v68, v206, v84, vcc
	v_cmp_le_i32_e32 vcc, v0, v131
	v_or_b32_e32 v0, 0x43, v129
	v_mfma_f32_32x32x16_bf16 v[18:33], v[172:175], v[74:77], v[18:33]
	v_cndmask_b32_e32 v52, v206, v100, vcc
	v_cmp_le_i32_e32 vcc, v0, v131
	v_or_b32_e32 v0, 0x63, v129
	s_nop 0
	v_cndmask_b32_e32 v69, v206, v85, vcc
	v_cmp_le_i32_e32 vcc, v0, v131
	v_or_b32_e32 v0, 0x48, v129
	v_max3_f32 v82, v68, v69, v51
	s_nop 0
	v_cndmask_b32_e32 v53, v206, v101, vcc
	v_cmp_le_i32_e32 vcc, v0, v131
	v_or_b32_e32 v0, 0x68, v129
	s_nop 0
	v_cndmask_b32_e32 v70, v206, v86, vcc
	v_cmp_le_i32_e32 vcc, v0, v131
	v_or_b32_e32 v0, 0x49, v129
	s_nop 0
	v_cndmask_b32_e32 v54, v206, v102, vcc
	v_cmp_le_i32_e32 vcc, v0, v131
	v_or_b32_e32 v0, 0x69, v129
	s_nop 0
	v_cndmask_b32_e32 v71, v206, v87, vcc
	v_cmp_le_i32_e32 vcc, v0, v131
	v_or_b32_e32 v0, 0x4a, v129
	s_nop 0
	v_cndmask_b32_e32 v55, v206, v103, vcc
	v_cmp_le_i32_e32 vcc, v0, v131
	v_or_b32_e32 v0, 0x6a, v129
	s_nop 0
	v_cndmask_b32_e32 v72, v206, v88, vcc
	v_cmp_le_i32_e32 vcc, v0, v131
	v_or_b32_e32 v0, 0x4b, v129
	s_nop 0
	v_cndmask_b32_e32 v56, v206, v104, vcc
	v_cmp_le_i32_e32 vcc, v0, v131
	v_or_b32_e32 v0, 0x6b, v129
	s_nop 0
	v_cndmask_b32_e32 v73, v206, v89, vcc
	v_cmp_le_i32_e32 vcc, v0, v131
	v_or_b32_e32 v0, 0x50, v129
	v_max3_f32 v82, v82, v72, v73
	s_nop 0
	v_cndmask_b32_e32 v57, v206, v105, vcc
	v_cmp_le_i32_e32 vcc, v0, v131
	v_or_b32_e32 v0, 0x70, v129
	v_max3_f32 v82, v82, v56, v57
	s_nop 0
	v_cndmask_b32_e32 v74, v206, v90, vcc
	v_cmp_le_i32_e32 vcc, v0, v131
	v_or_b32_e32 v0, 0x51, v129
	s_nop 0
	v_cndmask_b32_e32 v58, v206, v106, vcc
	v_cmp_le_i32_e32 vcc, v0, v131
	v_or_b32_e32 v0, 0x71, v129
	s_nop 0
	v_cndmask_b32_e32 v75, v206, v91, vcc
	v_cmp_le_i32_e32 vcc, v0, v131
	v_or_b32_e32 v0, 0x52, v129
	s_nop 0
	v_cndmask_b32_e32 v59, v206, v107, vcc
	v_cmp_le_i32_e32 vcc, v0, v131
	v_or_b32_e32 v0, 0x72, v129
	s_nop 0
	v_cndmask_b32_e32 v76, v206, v92, vcc
	v_cmp_le_i32_e32 vcc, v0, v131
	v_or_b32_e32 v0, 0x53, v129
	s_nop 0
	v_cndmask_b32_e32 v60, v206, v108, vcc
	v_cmp_le_i32_e32 vcc, v0, v131
	v_or_b32_e32 v0, 0x73, v129
	s_nop 0
	v_cndmask_b32_e32 v77, v206, v93, vcc
	v_cmp_le_i32_e32 vcc, v0, v131
	v_or_b32_e32 v0, 0x58, v129
	v_max3_f32 v82, v82, v76, v77
	s_nop 0
	v_cndmask_b32_e32 v61, v206, v109, vcc
	v_cmp_le_i32_e32 vcc, v0, v131
	v_or_b32_e32 v0, 0x78, v129
	v_max3_f32 v82, v82, v60, v61
	s_nop 0
	v_cndmask_b32_e32 v78, v206, v94, vcc
	v_cmp_le_i32_e32 vcc, v0, v131
	v_or_b32_e32 v0, 0x59, v129
	s_nop 0
	v_cndmask_b32_e32 v62, v206, v110, vcc
	v_cmp_le_i32_e32 vcc, v0, v131
	v_or_b32_e32 v0, 0x79, v129
	s_nop 0
	v_cndmask_b32_e32 v79, v206, v95, vcc
	v_cmp_le_i32_e32 vcc, v0, v131
	v_or_b32_e32 v0, 0x5a, v129
	s_nop 0
	v_cndmask_b32_e32 v63, v206, v111, vcc
	v_cmp_le_i32_e32 vcc, v0, v131
	v_or_b32_e32 v0, 0x7a, v129
	s_nop 0
	v_cndmask_b32_e32 v80, v206, v96, vcc
	v_cmp_le_i32_e32 vcc, v0, v131
	v_or_b32_e32 v0, 0x5b, v129
	s_nop 0
	v_cndmask_b32_e32 v64, v206, v112, vcc
	v_cmp_le_i32_e32 vcc, v0, v131
	v_or_b32_e32 v0, 0x7b, v129
	s_nop 0
	v_cndmask_b32_e32 v81, v206, v97, vcc
	v_cmp_le_i32_e32 vcc, v0, v131
	v_max3_f32 v0, v66, v67, v50
	v_max3_f32 v82, v82, v80, v81
	s_nop 0
	v_max3_f32 v0, v0, v52, v53
	s_nop 0
	v_max3_f32 v0, v0, v70, v71
	v_cndmask_b32_e32 v65, v206, v113, vcc
	v_max3_f32 v0, v0, v54, v55
	v_max3_f32 v82, v82, v64, v65
	s_nop 0
	v_max3_f32 v0, v0, v74, v75
	v_max_f32_e32 v82, v82, v82
	v_max3_f32 v0, v0, v58, v59
	s_nop 0
	v_max3_f32 v0, v0, v78, v79
	s_nop 0
	v_max3_f32 v0, v0, v62, v63
	s_nop 0
	v_max_f32_e32 v0, v0, v0
	v_max_f32_e32 v0, v0, v82
	v_mov_b32_e32 v82, v0
	s_nop 1
	v_permlane32_swap_b32_e32 v0, v82
	v_max_f32_e32 v82, v82, v82
	v_max_f32_e32 v0, v0, v0
	v_max_f32_e32 v0, v0, v82
	v_cmp_lt_f32_e32 vcc, s54, v0
	s_cbranch_vccnz .LBB0_1226
.LBB0_1179:
	s_waitcnt vmcnt(3) lgkmcnt(0)
	s_barrier
	s_setprio 1
	ds_read_b128 v[98:101], v132
	ds_read_b128 v[134:137], v132 offset:512
	v_exp_f32_e32 v66, v66
	v_exp_f32_e32 v67, v67
	v_exp_f32_e32 v68, v68
	v_exp_f32_e32 v69, v69
	s_nop 0
	v_exp_f32_e32 v70, v70
	v_exp_f32_e32 v71, v71
	v_exp_f32_e32 v72, v72
	v_exp_f32_e32 v73, v73
	ds_read_b128 v[138:141], v132 offset:2048
	ds_read_b128 v[142:145], v132 offset:2560
	v_exp_f32_e32 v74, v74
	v_exp_f32_e32 v75, v75
	v_exp_f32_e32 v76, v76
	v_exp_f32_e32 v77, v77
	s_waitcnt lgkmcnt(3)
	v_mfma_f32_32x32x16_bf16 v[82:97], v[98:101], v[196:199], v[34:49]
	s_nop 0
	v_exp_f32_e32 v78, v78
	v_exp_f32_e32 v79, v79
	v_exp_f32_e32 v80, v80
	v_exp_f32_e32 v81, v81
	s_waitcnt lgkmcnt(2)
	v_mfma_f32_32x32x16_bf16 v[98:113], v[134:137], v[196:199], v[34:49]
	v_add_f32_e32 v0, 0, v66
	v_add_f32_e32 v0, v67, v0
	v_add_f32_e32 v0, v68, v0
	v_add_f32_e32 v0, v69, v0
	ds_read_b128 v[134:137], v132 offset:4096
	ds_read_b128 v[146:149], v132 offset:4608
	v_add_f32_e32 v0, v0, v70
	v_add_f32_e32 v0, v71, v0
	v_add_f32_e32 v0, v72, v0
	v_exp_f32_e32 v50, v50
	v_exp_f32_e32 v51, v51
	v_exp_f32_e32 v52, v52
	v_exp_f32_e32 v53, v53
	v_add_f32_e32 v0, v73, v0
	s_waitcnt lgkmcnt(3)
	v_mfma_f32_32x32x16_bf16 v[82:97], v[138:141], v[192:195], v[82:97]
	s_nop 0
	v_add_f32_e32 v0, v74, v0
	v_add_f32_e32 v0, v75, v0
	v_add_f32_e32 v0, v76, v0
	v_exp_f32_e32 v54, v54
	v_exp_f32_e32 v55, v55
	v_exp_f32_e32 v56, v56
	v_exp_f32_e32 v57, v57
	v_add_f32_e32 v0, v77, v0
	v_cvt_pk_bf16_f32 v160, v66, v67
	v_cvt_pk_bf16_f32 v161, v68, v69
	s_waitcnt lgkmcnt(2)
	v_mfma_f32_32x32x16_bf16 v[98:113], v[142:145], v[192:195], v[98:113]
	ds_read_b128 v[66:69], v132 offset:6144
	ds_read_b128 v[138:141], v132 offset:6656
	v_add_f32_e32 v0, v78, v0
	v_add_f32_e32 v0, v79, v0
	v_add_f32_e32 v0, v80, v0
	v_exp_f32_e32 v58, v58
	v_exp_f32_e32 v59, v59
	v_exp_f32_e32 v60, v60
	v_exp_f32_e32 v61, v61
	v_add_f32_e32 v0, v81, v0
	v_cvt_pk_bf16_f32 v162, v70, v71
	v_cvt_pk_bf16_f32 v163, v72, v73
	s_waitcnt lgkmcnt(3)
	v_mfma_f32_32x32x16_bf16 v[82:97], v[134:137], v[188:191], v[82:97]
	s_nop 0
	v_exp_f32_e32 v62, v62
	v_exp_f32_e32 v63, v63
	v_exp_f32_e32 v64, v64
	v_exp_f32_e32 v65, v65
	v_cvt_pk_bf16_f32 v164, v74, v75
	v_add_f32_e32 v0, v0, v50
	v_add_f32_e32 v0, v51, v0
	v_add_f32_e32 v0, v52, v0
	v_add_f32_e32 v0, v53, v0
	v_cvt_pk_bf16_f32 v165, v76, v77
	s_waitcnt lgkmcnt(2)
	v_mfma_f32_32x32x16_bf16 v[98:113], v[146:149], v[188:191], v[98:113]
	ds_read_b128 v[70:73], v132 offset:8192
	ds_read_b128 v[74:77], v132 offset:8704
	v_add_f32_e32 v0, v0, v54
	v_add_f32_e32 v0, v55, v0
	v_add_f32_e32 v0, v56, v0
	v_add_f32_e32 v0, v57, v0
	v_cvt_pk_bf16_f32 v166, v78, v79
	v_cvt_pk_bf16_f32 v167, v80, v81
	s_waitcnt lgkmcnt(3)
	v_mfma_f32_32x32x16_bf16 v[82:97], v[66:69], v[184:187], v[82:97]
	s_nop 0
	v_add_f32_e32 v0, v58, v0
	v_add_f32_e32 v0, v59, v0
	v_add_f32_e32 v0, v60, v0
	v_add_f32_e32 v0, v61, v0
	v_cvt_pk_bf16_f32 v168, v50, v51
	v_cvt_pk_bf16_f32 v169, v52, v53
	s_waitcnt lgkmcnt(2)
	v_mfma_f32_32x32x16_bf16 v[98:113], v[138:141], v[184:187], v[98:113]
	ds_read_b128 v[50:53], v132 offset:10240
	ds_read_b128 v[66:69], v132 offset:10752
	v_add_f32_e32 v0, v62, v0
	v_add_f32_e32 v0, v63, v0
	v_add_f32_e32 v0, v64, v0
	v_add_f32_e32 v0, v65, v0
	v_cvt_pk_bf16_f32 v170, v54, v55
	v_cvt_pk_bf16_f32 v171, v56, v57
	s_waitcnt lgkmcnt(3)
	v_mfma_f32_32x32x16_bf16 v[82:97], v[70:73], v[180:183], v[82:97]
	v_cvt_pk_bf16_f32 v172, v58, v59
	v_cvt_pk_bf16_f32 v173, v60, v61
	s_waitcnt lgkmcnt(2)
	v_mfma_f32_32x32x16_bf16 v[98:113], v[74:77], v[180:183], v[98:113]
	v_cvt_pk_bf16_f32 v174, v62, v63
	v_cvt_pk_bf16_f32 v175, v64, v65
	s_waitcnt lgkmcnt(1)
	v_mfma_f32_32x32x16_bf16 v[82:97], v[50:53], v[176:179], v[82:97]
	s_waitcnt lgkmcnt(0)
	v_mfma_f32_32x32x16_bf16 v[98:113], v[66:69], v[176:179], v[98:113]
	v_add_f32_e32 v132, v133, v0
	s_setprio 0
	s_mov_b32 m0, s74
	v_lshl_add_u64 v[50:51], v[200:201], 0, s[0:1]
	global_load_lds_dwordx4 v[50:51], off
	s_xor_b32 s0, s73, 0x4000
	v_add_u32_e32 v0, s0, v211
	ds_read_b64_tr_b16 v[50:51],v0 offset:0
	ds_read_b64_tr_b16 v[52:53],v0 offset:512
	ds_read_b64_tr_b16 v[54:55],v0 offset:1024
	ds_read_b64_tr_b16 v[56:57],v0 offset:1536
	ds_read_b64_tr_b16 v[58:59],v0 offset:2048
	ds_read_b64_tr_b16 v[60:61],v0 offset:2560
	ds_read_b64_tr_b16 v[62:63],v0 offset:3072
	ds_read_b64_tr_b16 v[64:65],v0 offset:3584
	s_waitcnt lgkmcnt(0)
	s_nop 0
	v_mfma_f32_32x32x16_bf16 v[2:17], v[160:163], v[50:53], v[2:17]
	ds_read_b64_tr_b16 v[52:53],v0 offset:4096
	v_mfma_f32_32x32x16_bf16 v[2:17], v[164:167], v[54:57], v[2:17]
	ds_read_b64_tr_b16 v[54:55],v0 offset:4608
	ds_read_b64_tr_b16 v[56:57],v0 offset:5120
	v_mfma_f32_32x32x16_bf16 v[2:17], v[168:171], v[58:61], v[2:17]
	ds_read_b64_tr_b16 v[58:59],v0 offset:5632
	ds_read_b64_tr_b16 v[70:71],v0 offset:6144
	ds_read_b64_tr_b16 v[72:73],v0 offset:6656
	ds_read_b64_tr_b16 v[74:75],v0 offset:7168
	ds_read_b64_tr_b16 v[76:77],v0 offset:7680
	s_waitcnt lgkmcnt(0)
; __device__ __forceinline__ float max3f(float a, float b, float c) { float r; asm("v_max3_f32 %0, %1, %2, %3" : "=v"(r) : "v"(a), "v"(b), "v"(c)); return r; }
; __device__ __forceinline__ void cmask(f32x16& p0, f32x16& p1, int jb, int qrel, int hi) {
;     const float NEG = -INFINITY; const int kb = 64 * jb + 4 * hi;
; #pragma unroll
;     for (int r = 0; r < 16; ++r) { const int kv = kb + (r & 3) + 8 * (r >> 2); if (kv > qrel) p0[r] = NEG; if (kv + 32 > qrel) p1[r] = NEG; }
; }
; __device__ __forceinline__ float rowmax(const f32x16& p0, const f32x16& p1) {
;     float a = max3f(p0[0], p0[1], p1[0]), b = max3f(p0[2], p0[3], p1[1]); a = max3f(a, p1[2], p1[3]);
; #pragma unroll
;     for (int r = 4; r < 16; r += 4) { a = max3f(a, p0[r], p0[r + 1]); b = max3f(b, p0[r + 2], p0[r + 3]); a = max3f(a, p1[r], p1[r + 1]); b = max3f(b, p1[r + 2], p1[r + 3]); }
;     const float m = fmaxf(a, b);
;     auto rr = __builtin_amdgcn_permlane32_swap(__float_as_uint(m), __float_as_uint(m), false, false);
;     return fmaxf(__uint_as_float(rr[0]), __uint_as_float(rr[1]));
; }
; __device__ __forceinline__ void pv(f32x16* o, int vb, bf16x8 pa0, bf16x8 pa1, bf16x8 pa2, bf16x8 pa3) {
; #pragma unroll
;     for (int d0 = 0; d0 < 2; ++d0) { s16x4 lo[4], hi[4];
; #pragma unroll
;         for (int ks = 0; ks < 4; ++ks) {
;             asm volatile("ds_read_b64_tr_b16 %0,%1 offset:%c2" : "=&v"(lo[ks]) : "v"(vb), "i"(d0 * 4096 + ks * 1024) : "memory");
;             asm volatile("ds_read_b64_tr_b16 %0,%1 offset:%c2" : "=&v"(hi[ks]) : "v"(vb), "i"(d0 * 4096 + ks * 1024 + 512) : "memory"); }
;         asm volatile("s_waitcnt lgkmcnt(0)" ::: "memory"); __builtin_amdgcn_sched_barrier(0);
;     ...
;         o[d0] = __builtin_amdgcn_mfma_f32_32x32x16_bf16(pa0, MLA_PK(0), o[d0], 0, 0, 0);
;         o[d0] = __builtin_amdgcn_mfma_f32_32x32x16_bf16(pa1, MLA_PK(1), o[d0], 0, 0, 0);
;         o[d0] = __builtin_amdgcn_mfma_f32_32x32x16_bf16(pa2, MLA_PK(2), o[d0], 0, 0, 0);
;         o[d0] = __builtin_amdgcn_mfma_f32_32x32x16_bf16(pa3, MLA_PK(3), o[d0], 0, 0, 0);
;     ...
;     }
; }
	v_mfma_f32_32x32x16_bf16 v[2:17], v[172:175], v[62:65], v[2:17]
	v_mfma_f32_32x32x16_bf16 v[18:33], v[160:163], v[52:55], v[18:33]
	v_or_b32_e32 v50, 0xa0, v129
	v_or_b32_e32 v0, 0x80, v129
	v_cmp_le_i32_e32 vcc, v50, v131
	s_nop 1
	v_cndmask_b32_e32 v50, v206, v98, vcc
	v_cmp_lt_i32_e32 vcc, v0, v131
	v_mfma_f32_32x32x16_bf16 v[18:33], v[164:167], v[56:59], v[18:33]
	s_nop 0
	v_cndmask_b32_e32 v67, v206, v83, vcc
	v_cmp_le_i32_e32 vcc, v0, v131
	v_or_b32_e32 v0, 0xa1, v129
	s_nop 0
	v_cndmask_b32_e32 v66, v206, v82, vcc
	v_cmp_le_i32_e32 vcc, v0, v131
	v_or_b32_e32 v0, 0x82, v129
	v_mfma_f32_32x32x16_bf16 v[18:33], v[168:171], v[70:73], v[18:33]
	v_cndmask_b32_e32 v51, v206, v99, vcc
	v_cmp_le_i32_e32 vcc, v0, v131
	v_or_b32_e32 v0, 0xa2, v129
	s_nop 0
	v_cndmask_b32_e32 v68, v206, v84, vcc
	v_cmp_le_i32_e32 vcc, v0, v131
	v_or_b32_e32 v0, 0x83, v129
	v_mfma_f32_32x32x16_bf16 v[18:33], v[172:175], v[74:77], v[18:33]
	v_cndmask_b32_e32 v52, v206, v100, vcc
	v_cmp_le_i32_e32 vcc, v0, v131
	v_or_b32_e32 v0, 0xa3, v129
	s_nop 0
	v_cndmask_b32_e32 v69, v206, v85, vcc
	v_cmp_le_i32_e32 vcc, v0, v131
	v_or_b32_e32 v0, 0x88, v129
	v_max3_f32 v82, v68, v69, v51
	s_nop 0
	v_cndmask_b32_e32 v53, v206, v101, vcc
	v_cmp_le_i32_e32 vcc, v0, v131
	v_or_b32_e32 v0, 0xa8, v129
	s_nop 0
	v_cndmask_b32_e32 v70, v206, v86, vcc
	v_cmp_le_i32_e32 vcc, v0, v131
	v_or_b32_e32 v0, 0x89, v129
	s_nop 0
	v_cndmask_b32_e32 v54, v206, v102, vcc
	v_cmp_le_i32_e32 vcc, v0, v131
	v_or_b32_e32 v0, 0xa9, v129
	s_nop 0
	v_cndmask_b32_e32 v71, v206, v87, vcc
	v_cmp_le_i32_e32 vcc, v0, v131
	v_or_b32_e32 v0, 0x8a, v129
	s_nop 0
	v_cndmask_b32_e32 v55, v206, v103, vcc
	v_cmp_le_i32_e32 vcc, v0, v131
	v_or_b32_e32 v0, 0xaa, v129
	s_nop 0
	v_cndmask_b32_e32 v72, v206, v88, vcc
	v_cmp_le_i32_e32 vcc, v0, v131
	v_or_b32_e32 v0, 0x8b, v129
	s_nop 0
	v_cndmask_b32_e32 v56, v206, v104, vcc
	v_cmp_le_i32_e32 vcc, v0, v131
	v_or_b32_e32 v0, 0xab, v129
	s_nop 0
	v_cndmask_b32_e32 v73, v206, v89, vcc
	v_cmp_le_i32_e32 vcc, v0, v131
	v_or_b32_e32 v0, 0x90, v129
	v_max3_f32 v82, v82, v72, v73
	s_nop 0
	v_cndmask_b32_e32 v57, v206, v105, vcc
	v_cmp_le_i32_e32 vcc, v0, v131
	v_or_b32_e32 v0, 0xb0, v129
	v_max3_f32 v82, v82, v56, v57
	s_nop 0
	v_cndmask_b32_e32 v74, v206, v90, vcc
	v_cmp_le_i32_e32 vcc, v0, v131
	v_or_b32_e32 v0, 0x91, v129
	s_nop 0
	v_cndmask_b32_e32 v58, v206, v106, vcc
	v_cmp_le_i32_e32 vcc, v0, v131
	v_or_b32_e32 v0, 0xb1, v129
	s_nop 0
	v_cndmask_b32_e32 v75, v206, v91, vcc
	v_cmp_le_i32_e32 vcc, v0, v131
	v_or_b32_e32 v0, 0x92, v129
	s_nop 0
	v_cndmask_b32_e32 v59, v206, v107, vcc
	v_cmp_le_i32_e32 vcc, v0, v131
	v_or_b32_e32 v0, 0xb2, v129
	s_nop 0
	v_cndmask_b32_e32 v76, v206, v92, vcc
	v_cmp_le_i32_e32 vcc, v0, v131
	v_or_b32_e32 v0, 0x93, v129
	s_nop 0
	v_cndmask_b32_e32 v60, v206, v108, vcc
	v_cmp_le_i32_e32 vcc, v0, v131
	v_or_b32_e32 v0, 0xb3, v129
	s_nop 0
	v_cndmask_b32_e32 v77, v206, v93, vcc
	v_cmp_le_i32_e32 vcc, v0, v131
	v_or_b32_e32 v0, 0x98, v129
	v_max3_f32 v82, v82, v76, v77
	s_nop 0
	v_cndmask_b32_e32 v61, v206, v109, vcc
	v_cmp_le_i32_e32 vcc, v0, v131
	v_or_b32_e32 v0, 0xb8, v129
	v_max3_f32 v82, v82, v60, v61
	s_nop 0
	v_cndmask_b32_e32 v78, v206, v94, vcc
	v_cmp_le_i32_e32 vcc, v0, v131
	v_or_b32_e32 v0, 0x99, v129
	s_nop 0
	v_cndmask_b32_e32 v62, v206, v110, vcc
	v_cmp_le_i32_e32 vcc, v0, v131
	v_or_b32_e32 v0, 0xb9, v129
	s_nop 0
	v_cndmask_b32_e32 v79, v206, v95, vcc
	v_cmp_le_i32_e32 vcc, v0, v131
	v_or_b32_e32 v0, 0x9a, v129
	s_nop 0
	v_cndmask_b32_e32 v63, v206, v111, vcc
	v_cmp_le_i32_e32 vcc, v0, v131
	v_or_b32_e32 v0, 0xba, v129
	s_nop 0
	v_cndmask_b32_e32 v80, v206, v96, vcc
	v_cmp_le_i32_e32 vcc, v0, v131
	v_or_b32_e32 v0, 0x9b, v129
	s_nop 0
	v_cndmask_b32_e32 v64, v206, v112, vcc
	v_cmp_le_i32_e32 vcc, v0, v131
	v_or_b32_e32 v0, 0xbb, v129
	s_nop 0
	v_cndmask_b32_e32 v81, v206, v97, vcc
	v_cmp_le_i32_e32 vcc, v0, v131
	v_max3_f32 v0, v66, v67, v50
	v_max3_f32 v82, v82, v80, v81
	s_nop 0
	v_max3_f32 v0, v0, v52, v53
	s_nop 0
	v_max3_f32 v0, v0, v70, v71
	v_cndmask_b32_e32 v65, v206, v113, vcc
	v_max3_f32 v0, v0, v54, v55
	v_max3_f32 v82, v82, v64, v65
	s_nop 0
	v_max3_f32 v0, v0, v74, v75
	v_max_f32_e32 v82, v82, v82
	v_max3_f32 v0, v0, v58, v59
	s_nop 0
	v_max3_f32 v0, v0, v78, v79
	s_nop 0
	v_max3_f32 v0, v0, v62, v63
	s_nop 0
	v_max_f32_e32 v0, v0, v0
	v_max_f32_e32 v0, v0, v82
	v_mov_b32_e32 v82, v0
	s_nop 1
	v_permlane32_swap_b32_e32 v0, v82
	v_max_f32_e32 v82, v82, v82
	v_max_f32_e32 v0, v0, v0
	v_max_f32_e32 v0, v0, v82
	v_cmp_lt_f32_e32 vcc, s54, v0
	s_cbranch_vccnz .LBB0_1229

; template <int THRL, bool LATE> __device__ __forceinline__ void unit_stag(int b, int h, int qb, const unsigned short* Q, const unsigned short* KV, const unsigned short* KPE, unsigned short* O, char* shm, const int wave_) {
;     ...
;     glds16(ksrc, (unsigned)__builtin_amdgcn_readfirstlane(kdst)); if (lane < 32) glds16(psrc, (unsigned)__builtin_amdgcn_readfirstlane(pdst));
;     glds16(ksrc + (long)KVBLK * KVP, (unsigned)__builtin_amdgcn_readfirstlane(kdst + KSLOT)); if (lane < 32) glds16(psrc + (long)KVBLK * PEP, (unsigned)__builtin_amdgcn_readfirstlane(pdst + KSLOT)); glds16(vsrc, (unsigned)__builtin_amdgcn_readfirstlane(vdst));
;     glds16(ksrc + (long)2 * KVBLK * KVP, (unsigned)__builtin_amdgcn_readfirstlane(kdst + 2 * KSLOT)); if (lane < 32) glds16(psrc + (long)2 * KVBLK * PEP, (unsigned)__builtin_amdgcn_readfirstlane(pdst + 2 * KSLOT)); glds16(vsrc + (long)KVBLK * KVP, (unsigned)__builtin_amdgcn_readfirstlane(vdst + VSLOT));
.LBB0_1186:
	s_or_b64 exec, exec, s[40:41]
	s_lshl_b32 s40, s10, 4
	v_lshrrev_b32_e32 v0, 2, v96
	v_and_or_b32 v0, s40, 48, v0
	s_ashr_i32 s40, s45, 3
	s_andn2_b32 s40, s40, 31
	s_ashr_i32 s41, s40, 31
	v_lshlrev_b32_e32 v97, 3, v8
	v_lshlrev_b32_e32 v0, 11, v0
	v_and_b32_e32 v9, 24, v97
	v_lshl_add_u64 v[6:7], s[36:37], 0, v[0:1]
	s_cmp_lg_u32 0, -1
	v_lshl_add_u64 v[6:7], s[40:41], 1, v[6:7]
	v_lshlrev_b32_e32 v0, 1, v9
	s_cselect_b32 s40, 0, 0
	v_lshl_add_u64 v[6:7], v[6:7], 0, v[0:1]
	s_add_i32 s40, s40, s68
	s_add_i32 s44, s40, 0x9000
	s_mov_b32 m0, s44
	v_lshl_add_u64 v[6:7], v[6:7], 0, s[16:17]
	global_load_lds_dwordx4 v[6:7], off
	s_addk_i32 s40, 0x3000
	s_mov_b32 m0, s40
	v_lshl_add_u64 v[10:11], v[2:3], 0, s[12:13]
	global_load_lds_dwordx4 v[10:11], off
	s_and_saveexec_b64 s[40:41], s[2:3]
	s_cbranch_execz .LBB0_1188
	s_add_i32 s46, s42, 0x3000
	s_mov_b32 m0, s46
	v_lshl_add_u64 v[10:11], v[4:5], 0, s[14:15]
	global_load_lds_dwordx4 v[10:11], off
